# GEMM K-loops loop-edge edit: counter and carried-pointer SALU block moved in front of the closing barrier
# baseline (speedup 1.0000x reference)
;     ...
;         for (int t = 2; t < nt; t += 2) PG8_TRIP(t, false);
.LBB0_470:
	s_cmp_eq_u32 s67, 12
	s_cselect_b64 s[18:19], -1, 0
	s_and_b64 s[50:51], s[38:39], s[18:19]
	s_and_b64 s[18:19], s[50:51], exec
	s_cselect_b32 s19, s9, s35
	s_cselect_b32 s18, s8, s34
	s_add_u32 s42, s40, 0x100
	ds_read_b128 v[138:141], v134
	ds_read_b128 v[142:145], v134 offset:1024
	ds_read_b128 v[150:153], v134 offset:2048
	ds_read_b128 v[154:157], v134 offset:3072
	ds_read_b128 v[158:161], v135
	ds_read_b128 v[162:165], v135 offset:1024
	ds_read_b128 v[166:169], v135 offset:2048
	ds_read_b128 v[170:173], v135 offset:3072
	s_addc_u32 s43, s41, 0
	s_and_b32 s52, s42, 0x700
	s_add_u32 s18, s18, s52
	s_addc_u32 s19, s19, 0
	s_and_b64 s[50:51], s[50:51], exec
	s_cselect_b32 s53, s11, s31
	s_cselect_b32 s68, s10, s30
	s_add_u32 s50, s18, 0x80
	s_addc_u32 s51, s19, 0
	s_add_u32 s52, s68, s52
	s_addc_u32 s53, s53, 0
	s_add_u32 s40, s34, s40
	s_addc_u32 s41, s35, s41
	s_add_u32 s40, s40, 0x40080
	s_addc_u32 s41, s41, 0
	s_mov_b32 m0, s5
	ds_read_b128 v[174:177], v149
	ds_read_b128 v[178:181], v149 offset:1024
	ds_read_b128 v[182:185], v149 offset:2048
	ds_read_b128 v[186:189], v149 offset:3072
	ds_read_b128 v[194:197], v149 offset:4096
	ds_read_b128 v[198:201], v149 offset:5120
	ds_read_b128 v[202:205], v149 offset:6144
	ds_read_b128 v[206:209], v149 offset:7168
	s_nop 0
	v_lshl_add_u64 v[214:215], s[40:41], 0, v[132:133]
	global_load_lds_dwordx4 v[214:215], off
	v_lshl_add_u64 v[214:215], s[40:41], 0, v[130:131]
	s_mov_b32 m0, s7
	s_nop 0
	global_load_lds_dwordx4 v[214:215], off
	s_waitcnt vmcnt(8)
	s_waitcnt lgkmcnt(0)
	s_barrier
	s_setprio 1
	s_waitcnt lgkmcnt(0)
	v_mfma_f32_16x16x32_bf16 v[122:125], v[138:141], v[174:177], v[122:125]
	v_mfma_f32_16x16x32_bf16 v[114:117], v[150:153], v[174:177], v[114:117]
	v_mfma_f32_16x16x32_bf16 v[106:109], v[138:141], v[182:185], v[106:109]
	v_mfma_f32_16x16x32_bf16 v[98:101], v[150:153], v[182:185], v[98:101]
	v_mfma_f32_16x16x32_bf16 v[86:89], v[138:141], v[194:197], v[86:89]
	v_mfma_f32_16x16x32_bf16 v[70:73], v[150:153], v[194:197], v[70:73]
	v_mfma_f32_16x16x32_bf16 v[54:57], v[138:141], v[202:205], v[54:57]
	v_mfma_f32_16x16x32_bf16 v[38:41], v[150:153], v[202:205], v[38:41]
	v_mfma_f32_16x16x32_bf16 v[122:125], v[142:145], v[178:181], v[122:125]
	v_mfma_f32_16x16x32_bf16 v[114:117], v[154:157], v[178:181], v[114:117]
	v_mfma_f32_16x16x32_bf16 v[106:109], v[142:145], v[186:189], v[106:109]
	v_mfma_f32_16x16x32_bf16 v[98:101], v[154:157], v[186:189], v[98:101]
	v_mfma_f32_16x16x32_bf16 v[86:89], v[142:145], v[198:201], v[86:89]
	v_mfma_f32_16x16x32_bf16 v[70:73], v[154:157], v[198:201], v[70:73]
	v_mfma_f32_16x16x32_bf16 v[54:57], v[142:145], v[206:209], v[54:57]
	v_mfma_f32_16x16x32_bf16 v[38:41], v[154:157], v[206:209], v[38:41]
	s_setprio 0
	s_setprio 1
	v_mfma_f32_16x16x32_bf16 v[126:129], v[158:161], v[174:177], v[126:129]
	v_mfma_f32_16x16x32_bf16 v[118:121], v[166:169], v[174:177], v[118:121]
	v_mfma_f32_16x16x32_bf16 v[110:113], v[158:161], v[182:185], v[110:113]
	v_mfma_f32_16x16x32_bf16 v[102:105], v[166:169], v[182:185], v[102:105]
	v_mfma_f32_16x16x32_bf16 v[90:93], v[158:161], v[194:197], v[90:93]
	v_mfma_f32_16x16x32_bf16 v[74:77], v[166:169], v[194:197], v[74:77]
	v_mfma_f32_16x16x32_bf16 v[62:65], v[158:161], v[202:205], v[62:65]
	v_mfma_f32_16x16x32_bf16 v[50:53], v[166:169], v[202:205], v[50:53]
	v_mfma_f32_16x16x32_bf16 v[126:129], v[162:165], v[178:181], v[126:129]
	v_mfma_f32_16x16x32_bf16 v[118:121], v[170:173], v[178:181], v[118:121]
	v_mfma_f32_16x16x32_bf16 v[110:113], v[162:165], v[186:189], v[110:113]
	v_mfma_f32_16x16x32_bf16 v[102:105], v[170:173], v[186:189], v[102:105]
	v_mfma_f32_16x16x32_bf16 v[90:93], v[162:165], v[198:201], v[90:93]
	v_mfma_f32_16x16x32_bf16 v[74:77], v[170:173], v[198:201], v[74:77]
	v_mfma_f32_16x16x32_bf16 v[62:65], v[162:165], v[206:209], v[62:65]
	v_mfma_f32_16x16x32_bf16 v[50:53], v[170:173], v[206:209], v[50:53]
	s_setprio 0
	s_barrier
	s_mov_b64 s[40:41], s[52:53]
	s_mov_b32 m0, s61
	ds_read_b128 v[174:177], v149 offset:16384
	ds_read_b128 v[178:181], v149 offset:17408
	ds_read_b128 v[182:185], v149 offset:18432
	ds_read_b128 v[186:189], v149 offset:19456
	ds_read_b128 v[194:197], v149 offset:20480
	ds_read_b128 v[198:201], v149 offset:21504
	ds_read_b128 v[202:205], v149 offset:22528
	ds_read_b128 v[206:209], v149 offset:23552
	s_nop 0
	v_lshl_add_u64 v[214:215], s[40:41], 0, v[132:133]
	global_load_lds_dwordx4 v[214:215], off
	v_lshl_add_u64 v[214:215], s[40:41], 0, v[130:131]
	s_add_u32 s40, s52, 0x40000
	s_mov_b32 m0, s46
	s_addc_u32 s41, s53, 0
	global_load_lds_dwordx4 v[214:215], off
	s_mov_b32 m0, s47
	v_lshl_add_u64 v[214:215], s[40:41], 0, v[132:133]
	global_load_lds_dwordx4 v[214:215], off
	v_lshl_add_u64 v[214:215], s[40:41], 0, v[130:131]
	s_mov_b32 m0, s62
	s_mov_b64 s[40:41], s[18:19]
	global_load_lds_dwordx4 v[214:215], off
	s_mov_b32 m0, s23
	v_lshl_add_u64 v[214:215], s[40:41], 0, v[132:133]
	global_load_lds_dwordx4 v[214:215], off
	v_lshl_add_u64 v[214:215], s[40:41], 0, v[130:131]
	s_mov_b32 m0, s29
	s_nop 0
	global_load_lds_dwordx4 v[214:215], off
	s_waitcnt vmcnt(8)
	s_waitcnt lgkmcnt(0)
	s_barrier
	s_setprio 1
	s_waitcnt lgkmcnt(0)
	v_mfma_f32_16x16x32_bf16 v[94:97], v[138:141], v[174:177], v[94:97]
	v_mfma_f32_16x16x32_bf16 v[82:85], v[150:153], v[174:177], v[82:85]
	v_mfma_f32_16x16x32_bf16 v[58:61], v[138:141], v[182:185], v[58:61]
	v_mfma_f32_16x16x32_bf16 v[46:49], v[150:153], v[182:185], v[46:49]
	v_mfma_f32_16x16x32_bf16 v[30:33], v[138:141], v[194:197], v[30:33]
	v_mfma_f32_16x16x32_bf16 v[26:29], v[150:153], v[194:197], v[26:29]
	v_mfma_f32_16x16x32_bf16 v[14:17], v[138:141], v[202:205], v[14:17]
	v_mfma_f32_16x16x32_bf16 v[10:13], v[150:153], v[202:205], v[10:13]
	v_mfma_f32_16x16x32_bf16 v[94:97], v[142:145], v[178:181], v[94:97]
	v_mfma_f32_16x16x32_bf16 v[82:85], v[154:157], v[178:181], v[82:85]
	v_mfma_f32_16x16x32_bf16 v[58:61], v[142:145], v[186:189], v[58:61]
	v_mfma_f32_16x16x32_bf16 v[46:49], v[154:157], v[186:189], v[46:49]
	v_mfma_f32_16x16x32_bf16 v[30:33], v[142:145], v[198:201], v[30:33]
	v_mfma_f32_16x16x32_bf16 v[26:29], v[154:157], v[198:201], v[26:29]
	v_mfma_f32_16x16x32_bf16 v[14:17], v[142:145], v[206:209], v[14:17]
	v_mfma_f32_16x16x32_bf16 v[10:13], v[154:157], v[206:209], v[10:13]
	s_setprio 0
	s_setprio 1
	v_mfma_f32_16x16x32_bf16 v[78:81], v[158:161], v[174:177], v[78:81]
	v_mfma_f32_16x16x32_bf16 v[66:69], v[166:169], v[174:177], v[66:69]
	v_mfma_f32_16x16x32_bf16 v[42:45], v[158:161], v[182:185], v[42:45]
	v_mfma_f32_16x16x32_bf16 v[34:37], v[166:169], v[182:185], v[34:37]
	v_mfma_f32_16x16x32_bf16 v[22:25], v[158:161], v[194:197], v[22:25]
	v_mfma_f32_16x16x32_bf16 v[18:21], v[166:169], v[194:197], v[18:21]
	v_mfma_f32_16x16x32_bf16 v[6:9], v[158:161], v[202:205], v[6:9]
	v_mfma_f32_16x16x32_bf16 v[2:5], v[166:169], v[202:205], v[2:5]
	v_mfma_f32_16x16x32_bf16 v[78:81], v[162:165], v[178:181], v[78:81]
	v_mfma_f32_16x16x32_bf16 v[66:69], v[170:173], v[178:181], v[66:69]
	v_mfma_f32_16x16x32_bf16 v[42:45], v[162:165], v[186:189], v[42:45]
	v_mfma_f32_16x16x32_bf16 v[34:37], v[170:173], v[186:189], v[34:37]
	v_mfma_f32_16x16x32_bf16 v[22:25], v[162:165], v[198:201], v[22:25]
	v_mfma_f32_16x16x32_bf16 v[18:21], v[170:173], v[198:201], v[18:21]
	v_mfma_f32_16x16x32_bf16 v[6:9], v[162:165], v[206:209], v[6:9]
	v_mfma_f32_16x16x32_bf16 v[2:5], v[170:173], v[206:209], v[2:5]
	s_setprio 0
	s_barrier
	ds_read_b128 v[138:141], v136
	ds_read_b128 v[142:145], v136 offset:1024
	ds_read_b128 v[150:153], v136 offset:2048
	ds_read_b128 v[154:157], v136 offset:3072
	ds_read_b128 v[158:161], v137
	ds_read_b128 v[162:165], v137 offset:1024
	ds_read_b128 v[166:169], v137 offset:2048
	ds_read_b128 v[170:173], v137 offset:3072
	s_add_u32 s18, s18, 0x40000
	s_addc_u32 s19, s19, 0
	s_mov_b32 m0, s55
	ds_read_b128 v[174:177], v149 offset:32768
	ds_read_b128 v[178:181], v149 offset:33792
	ds_read_b128 v[182:185], v149 offset:34816
	ds_read_b128 v[186:189], v149 offset:35840
	ds_read_b128 v[194:197], v149 offset:36864
	ds_read_b128 v[198:201], v149 offset:37888
	ds_read_b128 v[202:205], v149 offset:38912
	ds_read_b128 v[206:209], v149 offset:39936
	s_nop 0
	v_lshl_add_u64 v[214:215], s[18:19], 0, v[132:133]
	global_load_lds_dwordx4 v[214:215], off
	v_lshl_add_u64 v[214:215], s[18:19], 0, v[130:131]
	s_mov_b32 m0, s56
	s_nop 0
	global_load_lds_dwordx4 v[214:215], off
	s_waitcnt vmcnt(8)
	s_waitcnt lgkmcnt(0)
	s_barrier
	s_setprio 1
	s_waitcnt lgkmcnt(0)
	v_mfma_f32_16x16x32_bf16 v[122:125], v[138:141], v[174:177], v[122:125]
	v_mfma_f32_16x16x32_bf16 v[114:117], v[150:153], v[174:177], v[114:117]
	v_mfma_f32_16x16x32_bf16 v[106:109], v[138:141], v[182:185], v[106:109]
	v_mfma_f32_16x16x32_bf16 v[98:101], v[150:153], v[182:185], v[98:101]
	v_mfma_f32_16x16x32_bf16 v[86:89], v[138:141], v[194:197], v[86:89]
	v_mfma_f32_16x16x32_bf16 v[70:73], v[150:153], v[194:197], v[70:73]
	v_mfma_f32_16x16x32_bf16 v[54:57], v[138:141], v[202:205], v[54:57]
	v_mfma_f32_16x16x32_bf16 v[38:41], v[150:153], v[202:205], v[38:41]
	v_mfma_f32_16x16x32_bf16 v[122:125], v[142:145], v[178:181], v[122:125]
	v_mfma_f32_16x16x32_bf16 v[114:117], v[154:157], v[178:181], v[114:117]
	v_mfma_f32_16x16x32_bf16 v[106:109], v[142:145], v[186:189], v[106:109]
	v_mfma_f32_16x16x32_bf16 v[98:101], v[154:157], v[186:189], v[98:101]
	v_mfma_f32_16x16x32_bf16 v[86:89], v[142:145], v[198:201], v[86:89]
	v_mfma_f32_16x16x32_bf16 v[70:73], v[154:157], v[198:201], v[70:73]
	v_mfma_f32_16x16x32_bf16 v[54:57], v[142:145], v[206:209], v[54:57]
	v_mfma_f32_16x16x32_bf16 v[38:41], v[154:157], v[206:209], v[38:41]
	s_setprio 0
	s_setprio 1
	v_mfma_f32_16x16x32_bf16 v[126:129], v[158:161], v[174:177], v[126:129]
	v_mfma_f32_16x16x32_bf16 v[118:121], v[166:169], v[174:177], v[118:121]
	v_mfma_f32_16x16x32_bf16 v[110:113], v[158:161], v[182:185], v[110:113]
	v_mfma_f32_16x16x32_bf16 v[102:105], v[166:169], v[182:185], v[102:105]
	v_mfma_f32_16x16x32_bf16 v[90:93], v[158:161], v[194:197], v[90:93]
	v_mfma_f32_16x16x32_bf16 v[74:77], v[166:169], v[194:197], v[74:77]
	v_mfma_f32_16x16x32_bf16 v[62:65], v[158:161], v[202:205], v[62:65]
	v_mfma_f32_16x16x32_bf16 v[50:53], v[166:169], v[202:205], v[50:53]
	v_mfma_f32_16x16x32_bf16 v[126:129], v[162:165], v[178:181], v[126:129]
	v_mfma_f32_16x16x32_bf16 v[118:121], v[170:173], v[178:181], v[118:121]
	v_mfma_f32_16x16x32_bf16 v[110:113], v[162:165], v[186:189], v[110:113]
	v_mfma_f32_16x16x32_bf16 v[102:105], v[170:173], v[186:189], v[102:105]
	v_mfma_f32_16x16x32_bf16 v[90:93], v[162:165], v[198:201], v[90:93]
	v_mfma_f32_16x16x32_bf16 v[74:77], v[170:173], v[198:201], v[74:77]
	v_mfma_f32_16x16x32_bf16 v[62:65], v[162:165], v[206:209], v[62:65]
	v_mfma_f32_16x16x32_bf16 v[50:53], v[170:173], v[206:209], v[50:53]
	s_setprio 0
	s_barrier
;     ...
;         for (int t = 2; t < nt; t += 2) PG8_TRIP(t, false);
	s_add_u32 s18, s52, 0x80
	s_addc_u32 s19, s53, 0
	s_mov_b32 m0, s63
	ds_read_b128 v[174:177], v149 offset:49152
	ds_read_b128 v[178:181], v149 offset:50176
	ds_read_b128 v[182:185], v149 offset:51200
	ds_read_b128 v[186:189], v149 offset:52224
	ds_read_b128 v[194:197], v149 offset:53248
	ds_read_b128 v[198:201], v149 offset:54272
	ds_read_b128 v[202:205], v149 offset:55296
	ds_read_b128 v[206:209], v149 offset:56320
	s_nop 0
	v_lshl_add_u64 v[214:215], s[18:19], 0, v[132:133]
	global_load_lds_dwordx4 v[214:215], off
	v_lshl_add_u64 v[214:215], s[18:19], 0, v[130:131]
	s_add_u32 s18, s52, 0x40080
	s_mov_b32 m0, s64
	s_addc_u32 s19, s53, 0
	global_load_lds_dwordx4 v[214:215], off
	s_mov_b32 m0, s65
	v_lshl_add_u64 v[214:215], s[18:19], 0, v[132:133]
	global_load_lds_dwordx4 v[214:215], off
	v_lshl_add_u64 v[214:215], s[18:19], 0, v[130:131]
	s_mov_b32 m0, s66
	s_nop 0
	global_load_lds_dwordx4 v[214:215], off
	s_mov_b32 m0, s57
	v_lshl_add_u64 v[214:215], s[50:51], 0, v[132:133]
	global_load_lds_dwordx4 v[214:215], off
	v_lshl_add_u64 v[214:215], s[50:51], 0, v[130:131]
	s_mov_b32 m0, s58
	s_nop 0
	global_load_lds_dwordx4 v[214:215], off
	s_waitcnt vmcnt(8)
	s_waitcnt lgkmcnt(0)
	s_barrier
	s_setprio 1
	s_waitcnt lgkmcnt(0)
	v_mfma_f32_16x16x32_bf16 v[94:97], v[138:141], v[174:177], v[94:97]
	v_mfma_f32_16x16x32_bf16 v[82:85], v[150:153], v[174:177], v[82:85]
	v_mfma_f32_16x16x32_bf16 v[58:61], v[138:141], v[182:185], v[58:61]
	v_mfma_f32_16x16x32_bf16 v[46:49], v[150:153], v[182:185], v[46:49]
	v_mfma_f32_16x16x32_bf16 v[30:33], v[138:141], v[194:197], v[30:33]
	v_mfma_f32_16x16x32_bf16 v[26:29], v[150:153], v[194:197], v[26:29]
	v_mfma_f32_16x16x32_bf16 v[14:17], v[138:141], v[202:205], v[14:17]
	v_mfma_f32_16x16x32_bf16 v[10:13], v[150:153], v[202:205], v[10:13]
	v_mfma_f32_16x16x32_bf16 v[94:97], v[142:145], v[178:181], v[94:97]
	v_mfma_f32_16x16x32_bf16 v[82:85], v[154:157], v[178:181], v[82:85]
	v_mfma_f32_16x16x32_bf16 v[58:61], v[142:145], v[186:189], v[58:61]
	v_mfma_f32_16x16x32_bf16 v[46:49], v[154:157], v[186:189], v[46:49]
	v_mfma_f32_16x16x32_bf16 v[30:33], v[142:145], v[198:201], v[30:33]
	v_mfma_f32_16x16x32_bf16 v[26:29], v[154:157], v[198:201], v[26:29]
	v_mfma_f32_16x16x32_bf16 v[14:17], v[142:145], v[206:209], v[14:17]
	v_mfma_f32_16x16x32_bf16 v[10:13], v[154:157], v[206:209], v[10:13]
	s_setprio 0
	s_setprio 1
	v_mfma_f32_16x16x32_bf16 v[78:81], v[158:161], v[174:177], v[78:81]
	v_mfma_f32_16x16x32_bf16 v[66:69], v[166:169], v[174:177], v[66:69]
	v_mfma_f32_16x16x32_bf16 v[42:45], v[158:161], v[182:185], v[42:45]
	v_mfma_f32_16x16x32_bf16 v[34:37], v[166:169], v[182:185], v[34:37]
	v_mfma_f32_16x16x32_bf16 v[22:25], v[158:161], v[194:197], v[22:25]
	v_mfma_f32_16x16x32_bf16 v[18:21], v[166:169], v[194:197], v[18:21]
	v_mfma_f32_16x16x32_bf16 v[6:9], v[158:161], v[202:205], v[6:9]
	v_mfma_f32_16x16x32_bf16 v[2:5], v[166:169], v[202:205], v[2:5]
	v_mfma_f32_16x16x32_bf16 v[78:81], v[162:165], v[178:181], v[78:81]
	v_mfma_f32_16x16x32_bf16 v[66:69], v[170:173], v[178:181], v[66:69]
	v_mfma_f32_16x16x32_bf16 v[42:45], v[162:165], v[186:189], v[42:45]
	v_mfma_f32_16x16x32_bf16 v[34:37], v[170:173], v[186:189], v[34:37]
	v_mfma_f32_16x16x32_bf16 v[22:25], v[162:165], v[198:201], v[22:25]
	v_mfma_f32_16x16x32_bf16 v[18:21], v[170:173], v[198:201], v[18:21]
	v_mfma_f32_16x16x32_bf16 v[6:9], v[162:165], v[206:209], v[6:9]
	v_mfma_f32_16x16x32_bf16 v[2:5], v[170:173], v[206:209], v[2:5]
	s_add_i32 s67, s67, 2
	s_cmp_gt_u32 s67, 13
	s_mov_b64 s[40:41], s[42:43]
	s_setprio 0
	s_barrier
	s_cbranch_scc0 .LBB0_470
	s_and_b64 vcc, exec, s[2:3]
	s_cbranch_vccz .LBB0_473
	s_barrier

.LBB0_670:
	s_cmp_eq_u32 s72, 4
	s_cselect_b64 s[38:39], -1, 0
	s_and_b64 s[40:41], s[36:37], s[38:39]
	s_and_b64 s[38:39], s[40:41], exec
	s_cselect_b32 s42, s55, s29
	s_cselect_b32 s43, s54, s28
	s_add_u32 s38, s30, 0x100
	ds_read_b128 v[18:21], v173
	ds_read_b128 v[22:25], v173 offset:1024
	ds_read_b128 v[26:29], v173 offset:2048
	ds_read_b128 v[30:33], v173 offset:3072
	ds_read_b128 v[10:13], v174
	ds_read_b128 v[14:17], v174 offset:1024
	ds_read_b128 v[2:5], v174 offset:2048
	ds_read_b128 v[6:9], v174 offset:3072
	s_addc_u32 s39, s31, 0
	s_and_b32 s73, s38, 0x300
	s_add_u32 s58, s43, s73
	s_addc_u32 s59, s42, 0
	s_and_b64 s[40:41], s[40:41], exec
	s_cselect_b32 s43, s57, s9
	s_cselect_b32 s42, s56, s8
	s_add_u32 s40, s58, 0x80
	s_addc_u32 s41, s59, 0
	s_add_u32 s42, s42, s73
	s_addc_u32 s43, s43, 0
	s_add_u32 s30, s28, s30
	s_addc_u32 s31, s29, s31
	s_add_u32 s30, s30, 0x20080
	s_addc_u32 s31, s31, 0
	s_mov_b32 m0, s3
	ds_read_b128 v[178:181], v172
	ds_read_b128 v[182:185], v172 offset:1024
	ds_read_b128 v[194:197], v172 offset:2048
	ds_read_b128 v[198:201], v172 offset:3072
	ds_read_b128 v[214:217], v172 offset:4096
	ds_read_b128 v[218:221], v172 offset:5120
	ds_read_b128 v[222:225], v172 offset:6144
	ds_read_b128 v[226:229], v172 offset:7168
	s_nop 0
	v_lshl_add_u64 v[186:187], s[30:31], 0, v[162:163]
	global_load_lds_dwordx4 v[186:187], off
	v_lshl_add_u64 v[186:187], s[30:31], 0, v[164:165]
	s_mov_b32 m0, s7
	s_nop 0
	global_load_lds_dwordx4 v[186:187], off
	s_waitcnt vmcnt(8)
	s_waitcnt lgkmcnt(0)
	s_barrier
	s_setprio 1
	s_waitcnt lgkmcnt(0)
	v_mfma_f32_16x16x128_f8f6f4 v[146:149], v[18:25], v[178:185], v[146:149]
	v_mfma_f32_16x16x128_f8f6f4 v[150:153], v[26:33], v[178:185], v[150:153]
	v_mfma_f32_16x16x128_f8f6f4 v[134:137], v[18:25], v[194:201], v[134:137]
	v_mfma_f32_16x16x128_f8f6f4 v[130:133], v[26:33], v[194:201], v[130:133]
	v_mfma_f32_16x16x128_f8f6f4 v[118:121], v[18:25], v[214:221], v[118:121]
	v_mfma_f32_16x16x128_f8f6f4 v[114:117], v[26:33], v[214:221], v[114:117]
	v_mfma_f32_16x16x128_f8f6f4 v[102:105], v[18:25], v[222:229], v[102:105]
	v_mfma_f32_16x16x128_f8f6f4 v[98:101], v[26:33], v[222:229], v[98:101]
	s_setprio 0
	s_setprio 1
	v_mfma_f32_16x16x128_f8f6f4 v[154:157], v[10:17], v[178:185], v[154:157]
	v_mfma_f32_16x16x128_f8f6f4 v[158:161], v[2:9], v[178:185], v[158:161]
	v_mfma_f32_16x16x128_f8f6f4 v[142:145], v[10:17], v[194:201], v[142:145]
	v_mfma_f32_16x16x128_f8f6f4 v[138:141], v[2:9], v[194:201], v[138:141]
	v_mfma_f32_16x16x128_f8f6f4 v[126:129], v[10:17], v[214:221], v[126:129]
	v_mfma_f32_16x16x128_f8f6f4 v[122:125], v[2:9], v[214:221], v[122:125]
	v_mfma_f32_16x16x128_f8f6f4 v[110:113], v[10:17], v[222:229], v[110:113]
	v_mfma_f32_16x16x128_f8f6f4 v[106:109], v[2:9], v[222:229], v[106:109]
	s_setprio 0
	s_barrier
	s_mov_b64 s[30:31], s[42:43]
	s_mov_b32 m0, s12
	ds_read_b128 v[178:181], v172 offset:16384
	ds_read_b128 v[182:185], v172 offset:17408
	ds_read_b128 v[194:197], v172 offset:18432
	ds_read_b128 v[198:201], v172 offset:19456
	ds_read_b128 v[214:217], v172 offset:20480
	ds_read_b128 v[218:221], v172 offset:21504
	ds_read_b128 v[222:225], v172 offset:22528
	ds_read_b128 v[226:229], v172 offset:23552
	s_nop 0
	v_lshl_add_u64 v[186:187], s[30:31], 0, v[162:163]
	global_load_lds_dwordx4 v[186:187], off
	v_lshl_add_u64 v[186:187], s[30:31], 0, v[164:165]
	s_add_u32 s30, s42, 0x20000
	s_mov_b32 m0, s35
	s_addc_u32 s31, s43, 0
	global_load_lds_dwordx4 v[186:187], off
	s_mov_b32 m0, s53
	v_lshl_add_u64 v[186:187], s[30:31], 0, v[162:163]
	global_load_lds_dwordx4 v[186:187], off
	v_lshl_add_u64 v[186:187], s[30:31], 0, v[164:165]
	s_mov_b32 m0, s69
	s_mov_b64 s[30:31], s[58:59]
	global_load_lds_dwordx4 v[186:187], off
	s_mov_b32 m0, s46
	v_lshl_add_u64 v[186:187], s[30:31], 0, v[162:163]
	global_load_lds_dwordx4 v[186:187], off
	v_lshl_add_u64 v[186:187], s[30:31], 0, v[164:165]
	s_mov_b32 m0, s47
	s_nop 0
	global_load_lds_dwordx4 v[186:187], off
	s_waitcnt vmcnt(8)
	s_waitcnt lgkmcnt(0)
	s_barrier
	s_setprio 1
	s_waitcnt lgkmcnt(0)
	v_mfma_f32_16x16x128_f8f6f4 v[86:89], v[18:25], v[178:185], v[86:89]
	v_mfma_f32_16x16x128_f8f6f4 v[82:85], v[26:33], v[178:185], v[82:85]
	v_mfma_f32_16x16x128_f8f6f4 v[70:73], v[18:25], v[194:201], v[70:73]
	v_mfma_f32_16x16x128_f8f6f4 v[66:69], v[26:33], v[194:201], v[66:69]
	v_mfma_f32_16x16x128_f8f6f4 v[58:61], v[18:25], v[214:221], v[58:61]
	v_mfma_f32_16x16x128_f8f6f4 v[50:53], v[26:33], v[214:221], v[50:53]
	v_mfma_f32_16x16x128_f8f6f4 v[46:49], v[18:25], v[222:229], v[46:49]
	v_mfma_f32_16x16x128_f8f6f4 v[38:41], v[26:33], v[222:229], v[38:41]
	s_setprio 0
	s_setprio 1
	v_mfma_f32_16x16x128_f8f6f4 v[94:97], v[10:17], v[178:185], v[94:97]
	v_mfma_f32_16x16x128_f8f6f4 v[90:93], v[2:9], v[178:185], v[90:93]
	v_mfma_f32_16x16x128_f8f6f4 v[78:81], v[10:17], v[194:201], v[78:81]
	v_mfma_f32_16x16x128_f8f6f4 v[74:77], v[2:9], v[194:201], v[74:77]
	v_mfma_f32_16x16x128_f8f6f4 v[62:65], v[10:17], v[214:221], v[62:65]
	v_mfma_f32_16x16x128_f8f6f4 v[54:57], v[2:9], v[214:221], v[54:57]
	v_mfma_f32_16x16x128_f8f6f4 v[42:45], v[10:17], v[222:229], v[42:45]
	v_mfma_f32_16x16x128_f8f6f4 v[34:37], v[2:9], v[222:229], v[34:37]
	s_setprio 0
	s_barrier
;     ...
;         for (int t = 2; t < nt; t += 2) PG8_TRIP(t, false);
	ds_read_b128 v[26:29], v175
	ds_read_b128 v[30:33], v175 offset:1024
	ds_read_b128 v[18:21], v175 offset:2048
	ds_read_b128 v[22:25], v175 offset:3072
	ds_read_b128 v[10:13], v176
	ds_read_b128 v[14:17], v176 offset:1024
	ds_read_b128 v[2:5], v176 offset:2048
	ds_read_b128 v[6:9], v176 offset:3072
	s_add_u32 s30, s58, 0x20000
	s_addc_u32 s31, s59, 0
	s_mov_b32 m0, s61
	ds_read_b128 v[178:181], v172 offset:32768
	ds_read_b128 v[182:185], v172 offset:33792
	ds_read_b128 v[194:197], v172 offset:34816
	ds_read_b128 v[198:201], v172 offset:35840
	ds_read_b128 v[214:217], v172 offset:36864
	ds_read_b128 v[218:221], v172 offset:37888
	ds_read_b128 v[222:225], v172 offset:38912
	ds_read_b128 v[226:229], v172 offset:39936
	s_nop 0
	v_lshl_add_u64 v[186:187], s[30:31], 0, v[162:163]
	global_load_lds_dwordx4 v[186:187], off
	v_lshl_add_u64 v[186:187], s[30:31], 0, v[164:165]
	s_mov_b32 m0, s62
	s_nop 0
	global_load_lds_dwordx4 v[186:187], off
	s_waitcnt vmcnt(8)
	s_waitcnt lgkmcnt(0)
	s_barrier
	s_setprio 1
	s_waitcnt lgkmcnt(0)
	v_mfma_f32_16x16x128_f8f6f4 v[146:149], v[26:33], v[178:185], v[146:149]
	v_mfma_f32_16x16x128_f8f6f4 v[150:153], v[18:25], v[178:185], v[150:153]
	v_mfma_f32_16x16x128_f8f6f4 v[134:137], v[26:33], v[194:201], v[134:137]
	v_mfma_f32_16x16x128_f8f6f4 v[130:133], v[18:25], v[194:201], v[130:133]
	v_mfma_f32_16x16x128_f8f6f4 v[118:121], v[26:33], v[214:221], v[118:121]
	v_mfma_f32_16x16x128_f8f6f4 v[114:117], v[18:25], v[214:221], v[114:117]
	v_mfma_f32_16x16x128_f8f6f4 v[102:105], v[26:33], v[222:229], v[102:105]
	v_mfma_f32_16x16x128_f8f6f4 v[98:101], v[18:25], v[222:229], v[98:101]
	s_setprio 0
	s_setprio 1
	v_mfma_f32_16x16x128_f8f6f4 v[154:157], v[10:17], v[178:185], v[154:157]
	v_mfma_f32_16x16x128_f8f6f4 v[158:161], v[2:9], v[178:185], v[158:161]
	v_mfma_f32_16x16x128_f8f6f4 v[142:145], v[10:17], v[194:201], v[142:145]
	v_mfma_f32_16x16x128_f8f6f4 v[138:141], v[2:9], v[194:201], v[138:141]
	v_mfma_f32_16x16x128_f8f6f4 v[126:129], v[10:17], v[214:221], v[126:129]
	v_mfma_f32_16x16x128_f8f6f4 v[122:125], v[2:9], v[214:221], v[122:125]
	v_mfma_f32_16x16x128_f8f6f4 v[110:113], v[10:17], v[222:229], v[110:113]
	v_mfma_f32_16x16x128_f8f6f4 v[106:109], v[2:9], v[222:229], v[106:109]
	s_setprio 0
	s_barrier
	s_add_u32 s30, s42, 0x80
	s_addc_u32 s31, s43, 0
	s_mov_b32 m0, s18
	ds_read_b128 v[178:181], v172 offset:49152
	ds_read_b128 v[182:185], v172 offset:50176
	ds_read_b128 v[194:197], v172 offset:51200
	ds_read_b128 v[198:201], v172 offset:52224
	ds_read_b128 v[214:217], v172 offset:53248
	ds_read_b128 v[218:221], v172 offset:54272
	ds_read_b128 v[222:225], v172 offset:55296
	ds_read_b128 v[226:229], v172 offset:56320
	s_nop 0
	v_lshl_add_u64 v[186:187], s[30:31], 0, v[162:163]
	global_load_lds_dwordx4 v[186:187], off
	v_lshl_add_u64 v[186:187], s[30:31], 0, v[164:165]
	s_add_u32 s30, s42, 0x20080
	s_mov_b32 m0, s19
	s_addc_u32 s31, s43, 0
	global_load_lds_dwordx4 v[186:187], off
	s_mov_b32 m0, s70
	v_lshl_add_u64 v[186:187], s[30:31], 0, v[162:163]
	global_load_lds_dwordx4 v[186:187], off
	v_lshl_add_u64 v[186:187], s[30:31], 0, v[164:165]
	s_mov_b32 m0, s71
	s_nop 0
	global_load_lds_dwordx4 v[186:187], off
	s_mov_b32 m0, s65
	v_lshl_add_u64 v[186:187], s[40:41], 0, v[162:163]
	global_load_lds_dwordx4 v[186:187], off
	v_lshl_add_u64 v[186:187], s[40:41], 0, v[164:165]
	s_mov_b32 m0, s66
	s_nop 0
	global_load_lds_dwordx4 v[186:187], off
	s_waitcnt vmcnt(8)
	s_waitcnt lgkmcnt(0)
	s_barrier
	s_setprio 1
	s_waitcnt lgkmcnt(0)
	v_mfma_f32_16x16x128_f8f6f4 v[86:89], v[26:33], v[178:185], v[86:89]
	v_mfma_f32_16x16x128_f8f6f4 v[82:85], v[18:25], v[178:185], v[82:85]
	v_mfma_f32_16x16x128_f8f6f4 v[70:73], v[26:33], v[194:201], v[70:73]
	v_mfma_f32_16x16x128_f8f6f4 v[66:69], v[18:25], v[194:201], v[66:69]
	v_mfma_f32_16x16x128_f8f6f4 v[58:61], v[26:33], v[214:221], v[58:61]
	v_mfma_f32_16x16x128_f8f6f4 v[50:53], v[18:25], v[214:221], v[50:53]
	v_mfma_f32_16x16x128_f8f6f4 v[46:49], v[26:33], v[222:229], v[46:49]
	v_mfma_f32_16x16x128_f8f6f4 v[38:41], v[18:25], v[222:229], v[38:41]
	s_setprio 0
	s_setprio 1
	v_mfma_f32_16x16x128_f8f6f4 v[94:97], v[10:17], v[178:185], v[94:97]
	v_mfma_f32_16x16x128_f8f6f4 v[90:93], v[2:9], v[178:185], v[90:93]
	v_mfma_f32_16x16x128_f8f6f4 v[78:81], v[10:17], v[194:201], v[78:81]
	v_mfma_f32_16x16x128_f8f6f4 v[74:77], v[2:9], v[194:201], v[74:77]
	v_mfma_f32_16x16x128_f8f6f4 v[62:65], v[10:17], v[214:221], v[62:65]
	v_mfma_f32_16x16x128_f8f6f4 v[54:57], v[2:9], v[214:221], v[54:57]
	v_mfma_f32_16x16x128_f8f6f4 v[42:45], v[10:17], v[222:229], v[42:45]
	v_mfma_f32_16x16x128_f8f6f4 v[34:37], v[2:9], v[222:229], v[34:37]
	s_add_i32 s72, s72, 2
	s_cmp_gt_u32 s72, 5
	s_mov_b64 s[30:31], s[38:39]
	s_setprio 0
	s_barrier
	s_cbranch_scc0 .LBB0_670
	s_and_b64 vcc, exec, s[10:11]
	s_cbranch_vccz .LBB0_673
	s_barrier

.LBB0_1064:
	s_cmp_eq_u32 s65, 12
	s_cselect_b64 s[18:19], -1, 0
	s_and_b64 s[42:43], s[36:37], s[18:19]
	s_and_b64 s[18:19], s[42:43], exec
	s_cselect_b32 s19, s9, s35
	s_cselect_b32 s18, s8, s34
	s_add_u32 s40, s38, 0x100
	ds_read_b128 v[102:105], v98
	ds_read_b128 v[106:109], v98 offset:1024
	ds_read_b128 v[118:121], v98 offset:2048
	ds_read_b128 v[146:149], v98 offset:3072
	ds_read_b128 v[150:153], v99
	ds_read_b128 v[154:157], v99 offset:1024
	ds_read_b128 v[158:161], v99 offset:2048
	ds_read_b128 v[162:165], v99 offset:3072
	s_addc_u32 s41, s39, 0
	s_and_b32 s44, s40, 0x700
	s_add_u32 s18, s18, s44
	s_addc_u32 s19, s19, 0
	s_and_b64 s[42:43], s[42:43], exec
	s_cselect_b32 s45, s11, s31
	s_cselect_b32 s66, s10, s30
	s_add_u32 s42, s18, 0x80
	s_addc_u32 s43, s19, 0
	s_add_u32 s44, s66, s44
	s_addc_u32 s45, s45, 0
	s_add_u32 s38, s34, s38
	s_addc_u32 s39, s35, s39
	s_add_u32 s38, s38, 0x40080
	s_addc_u32 s39, s39, 0
	s_mov_b32 m0, s5
	ds_read_b128 v[166:169], v199
	ds_read_b128 v[170:173], v199 offset:1024
	ds_read_b128 v[174:177], v199 offset:2048
	ds_read_b128 v[178:181], v199 offset:3072
	ds_read_b128 v[184:187], v199 offset:4096
	ds_read_b128 v[194:197], v199 offset:5120
	ds_read_b128 v[200:203], v199 offset:6144
	ds_read_b128 v[204:207], v199 offset:7168
	s_nop 0
	v_lshl_add_u64 v[188:189], s[38:39], 0, v[190:191]
	global_load_lds_dwordx4 v[188:189], off
	v_lshl_add_u64 v[188:189], s[38:39], 0, v[182:183]
	s_mov_b32 m0, s7
	s_nop 0
	global_load_lds_dwordx4 v[188:189], off
	s_waitcnt vmcnt(8)
	s_waitcnt lgkmcnt(0)
	s_barrier
	s_setprio 1
	s_waitcnt lgkmcnt(0)
	v_mfma_f32_16x16x32_bf16 v[134:137], v[102:105], v[166:169], v[134:137]
	v_mfma_f32_16x16x32_bf16 v[142:145], v[118:121], v[166:169], v[142:145]
	v_mfma_f32_16x16x32_bf16 v[126:129], v[102:105], v[174:177], v[126:129]
	v_mfma_f32_16x16x32_bf16 v[122:125], v[118:121], v[174:177], v[122:125]
	v_mfma_f32_16x16x32_bf16 v[94:97], v[102:105], v[184:187], v[94:97]
	v_mfma_f32_16x16x32_bf16 v[90:93], v[118:121], v[184:187], v[90:93]
	v_mfma_f32_16x16x32_bf16 v[78:81], v[102:105], v[200:203], v[78:81]
	v_mfma_f32_16x16x32_bf16 v[70:73], v[118:121], v[200:203], v[70:73]
	v_mfma_f32_16x16x32_bf16 v[134:137], v[106:109], v[170:173], v[134:137]
	v_mfma_f32_16x16x32_bf16 v[142:145], v[146:149], v[170:173], v[142:145]
	v_mfma_f32_16x16x32_bf16 v[126:129], v[106:109], v[178:181], v[126:129]
	v_mfma_f32_16x16x32_bf16 v[122:125], v[146:149], v[178:181], v[122:125]
	v_mfma_f32_16x16x32_bf16 v[94:97], v[106:109], v[194:197], v[94:97]
	v_mfma_f32_16x16x32_bf16 v[90:93], v[146:149], v[194:197], v[90:93]
	v_mfma_f32_16x16x32_bf16 v[78:81], v[106:109], v[204:207], v[78:81]
	v_mfma_f32_16x16x32_bf16 v[70:73], v[146:149], v[204:207], v[70:73]
	s_setprio 0
	s_setprio 1
	v_mfma_f32_16x16x32_bf16 v[138:141], v[150:153], v[166:169], v[138:141]
	v_mfma_f32_16x16x32_bf16 v[130:133], v[158:161], v[166:169], v[130:133]
	v_mfma_f32_16x16x32_bf16 v[114:117], v[150:153], v[174:177], v[114:117]
	v_mfma_f32_16x16x32_bf16 v[110:113], v[158:161], v[174:177], v[110:113]
	v_mfma_f32_16x16x32_bf16 v[86:89], v[150:153], v[184:187], v[86:89]
	v_mfma_f32_16x16x32_bf16 v[82:85], v[158:161], v[184:187], v[82:85]
	v_mfma_f32_16x16x32_bf16 v[62:65], v[150:153], v[200:203], v[62:65]
	v_mfma_f32_16x16x32_bf16 v[54:57], v[158:161], v[200:203], v[54:57]
	v_mfma_f32_16x16x32_bf16 v[138:141], v[154:157], v[170:173], v[138:141]
	v_mfma_f32_16x16x32_bf16 v[130:133], v[162:165], v[170:173], v[130:133]
	v_mfma_f32_16x16x32_bf16 v[114:117], v[154:157], v[178:181], v[114:117]
	v_mfma_f32_16x16x32_bf16 v[110:113], v[162:165], v[178:181], v[110:113]
	v_mfma_f32_16x16x32_bf16 v[86:89], v[154:157], v[194:197], v[86:89]
	v_mfma_f32_16x16x32_bf16 v[82:85], v[162:165], v[194:197], v[82:85]
	v_mfma_f32_16x16x32_bf16 v[62:65], v[154:157], v[204:207], v[62:65]
	v_mfma_f32_16x16x32_bf16 v[54:57], v[162:165], v[204:207], v[54:57]
	s_setprio 0
	s_barrier
	s_mov_b64 s[38:39], s[44:45]
	s_mov_b32 m0, s56
	ds_read_b128 v[166:169], v199 offset:16384
	ds_read_b128 v[170:173], v199 offset:17408
	ds_read_b128 v[174:177], v199 offset:18432
	ds_read_b128 v[178:181], v199 offset:19456
	ds_read_b128 v[184:187], v199 offset:20480
	ds_read_b128 v[194:197], v199 offset:21504
	ds_read_b128 v[200:203], v199 offset:22528
	ds_read_b128 v[204:207], v199 offset:23552
	s_nop 0
	v_lshl_add_u64 v[188:189], s[38:39], 0, v[190:191]
	global_load_lds_dwordx4 v[188:189], off
	v_lshl_add_u64 v[188:189], s[38:39], 0, v[182:183]
	s_add_u32 s38, s44, 0x40000
	s_mov_b32 m0, s57
	s_addc_u32 s39, s45, 0
	global_load_lds_dwordx4 v[188:189], off
	s_mov_b32 m0, s58
	v_lshl_add_u64 v[188:189], s[38:39], 0, v[190:191]
	global_load_lds_dwordx4 v[188:189], off
	v_lshl_add_u64 v[188:189], s[38:39], 0, v[182:183]
	s_mov_b32 m0, s59
	s_mov_b64 s[38:39], s[18:19]
	global_load_lds_dwordx4 v[188:189], off
	s_mov_b32 m0, s23
	v_lshl_add_u64 v[188:189], s[38:39], 0, v[190:191]
	global_load_lds_dwordx4 v[188:189], off
	v_lshl_add_u64 v[188:189], s[38:39], 0, v[182:183]
	s_mov_b32 m0, s29
	s_nop 0
	global_load_lds_dwordx4 v[188:189], off
	s_waitcnt vmcnt(8)
	s_waitcnt lgkmcnt(0)
	s_barrier
	s_setprio 1
	s_waitcnt lgkmcnt(0)
	v_mfma_f32_16x16x32_bf16 v[74:77], v[102:105], v[166:169], v[74:77]
	v_mfma_f32_16x16x32_bf16 v[66:69], v[118:121], v[166:169], v[66:69]
	v_mfma_f32_16x16x32_bf16 v[46:49], v[102:105], v[174:177], v[46:49]
	v_mfma_f32_16x16x32_bf16 v[42:45], v[118:121], v[174:177], v[42:45]
	v_mfma_f32_16x16x32_bf16 v[30:33], v[102:105], v[184:187], v[30:33]
	v_mfma_f32_16x16x32_bf16 v[26:29], v[118:121], v[184:187], v[26:29]
	v_mfma_f32_16x16x32_bf16 v[14:17], v[102:105], v[200:203], v[14:17]
	v_mfma_f32_16x16x32_bf16 v[10:13], v[118:121], v[200:203], v[10:13]
	v_mfma_f32_16x16x32_bf16 v[74:77], v[106:109], v[170:173], v[74:77]
	v_mfma_f32_16x16x32_bf16 v[66:69], v[146:149], v[170:173], v[66:69]
	v_mfma_f32_16x16x32_bf16 v[46:49], v[106:109], v[178:181], v[46:49]
	v_mfma_f32_16x16x32_bf16 v[42:45], v[146:149], v[178:181], v[42:45]
	v_mfma_f32_16x16x32_bf16 v[30:33], v[106:109], v[194:197], v[30:33]
	v_mfma_f32_16x16x32_bf16 v[26:29], v[146:149], v[194:197], v[26:29]
	v_mfma_f32_16x16x32_bf16 v[14:17], v[106:109], v[204:207], v[14:17]
	v_mfma_f32_16x16x32_bf16 v[10:13], v[146:149], v[204:207], v[10:13]
	s_setprio 0
	s_setprio 1
	v_mfma_f32_16x16x32_bf16 v[58:61], v[150:153], v[166:169], v[58:61]
	v_mfma_f32_16x16x32_bf16 v[50:53], v[158:161], v[166:169], v[50:53]
	v_mfma_f32_16x16x32_bf16 v[38:41], v[150:153], v[174:177], v[38:41]
	v_mfma_f32_16x16x32_bf16 v[34:37], v[158:161], v[174:177], v[34:37]
	v_mfma_f32_16x16x32_bf16 v[22:25], v[150:153], v[184:187], v[22:25]
	v_mfma_f32_16x16x32_bf16 v[18:21], v[158:161], v[184:187], v[18:21]
	v_mfma_f32_16x16x32_bf16 v[6:9], v[150:153], v[200:203], v[6:9]
	v_mfma_f32_16x16x32_bf16 v[2:5], v[158:161], v[200:203], v[2:5]
	v_mfma_f32_16x16x32_bf16 v[58:61], v[154:157], v[170:173], v[58:61]
	v_mfma_f32_16x16x32_bf16 v[50:53], v[162:165], v[170:173], v[50:53]
	v_mfma_f32_16x16x32_bf16 v[38:41], v[154:157], v[178:181], v[38:41]
	v_mfma_f32_16x16x32_bf16 v[34:37], v[162:165], v[178:181], v[34:37]
	v_mfma_f32_16x16x32_bf16 v[22:25], v[154:157], v[194:197], v[22:25]
	v_mfma_f32_16x16x32_bf16 v[18:21], v[162:165], v[194:197], v[18:21]
	v_mfma_f32_16x16x32_bf16 v[6:9], v[154:157], v[204:207], v[6:9]
	v_mfma_f32_16x16x32_bf16 v[2:5], v[162:165], v[204:207], v[2:5]
	s_setprio 0
	s_barrier
	ds_read_b128 v[102:105], v100
	ds_read_b128 v[106:109], v100 offset:1024
	ds_read_b128 v[118:121], v100 offset:2048
	ds_read_b128 v[146:149], v100 offset:3072
	ds_read_b128 v[150:153], v101
	ds_read_b128 v[154:157], v101 offset:1024
	ds_read_b128 v[158:161], v101 offset:2048
	ds_read_b128 v[162:165], v101 offset:3072
	s_add_u32 s18, s18, 0x40000
	s_addc_u32 s19, s19, 0
	s_mov_b32 m0, s51
	ds_read_b128 v[166:169], v199 offset:32768
	ds_read_b128 v[170:173], v199 offset:33792
	ds_read_b128 v[174:177], v199 offset:34816
	ds_read_b128 v[178:181], v199 offset:35840
	ds_read_b128 v[184:187], v199 offset:36864
	ds_read_b128 v[194:197], v199 offset:37888
	ds_read_b128 v[200:203], v199 offset:38912
	ds_read_b128 v[204:207], v199 offset:39936
	s_nop 0
	v_lshl_add_u64 v[188:189], s[18:19], 0, v[190:191]
	global_load_lds_dwordx4 v[188:189], off
	v_lshl_add_u64 v[188:189], s[18:19], 0, v[182:183]
	s_mov_b32 m0, s52
	s_nop 0
	global_load_lds_dwordx4 v[188:189], off
	s_waitcnt vmcnt(8)
	s_waitcnt lgkmcnt(0)
	s_barrier
	s_setprio 1
	s_waitcnt lgkmcnt(0)
	v_mfma_f32_16x16x32_bf16 v[134:137], v[102:105], v[166:169], v[134:137]
	v_mfma_f32_16x16x32_bf16 v[142:145], v[118:121], v[166:169], v[142:145]
	v_mfma_f32_16x16x32_bf16 v[126:129], v[102:105], v[174:177], v[126:129]
	v_mfma_f32_16x16x32_bf16 v[122:125], v[118:121], v[174:177], v[122:125]
	v_mfma_f32_16x16x32_bf16 v[94:97], v[102:105], v[184:187], v[94:97]
	v_mfma_f32_16x16x32_bf16 v[90:93], v[118:121], v[184:187], v[90:93]
	v_mfma_f32_16x16x32_bf16 v[78:81], v[102:105], v[200:203], v[78:81]
	v_mfma_f32_16x16x32_bf16 v[70:73], v[118:121], v[200:203], v[70:73]
	v_mfma_f32_16x16x32_bf16 v[134:137], v[106:109], v[170:173], v[134:137]
	v_mfma_f32_16x16x32_bf16 v[142:145], v[146:149], v[170:173], v[142:145]
	v_mfma_f32_16x16x32_bf16 v[126:129], v[106:109], v[178:181], v[126:129]
	v_mfma_f32_16x16x32_bf16 v[122:125], v[146:149], v[178:181], v[122:125]
	v_mfma_f32_16x16x32_bf16 v[94:97], v[106:109], v[194:197], v[94:97]
	v_mfma_f32_16x16x32_bf16 v[90:93], v[146:149], v[194:197], v[90:93]
	v_mfma_f32_16x16x32_bf16 v[78:81], v[106:109], v[204:207], v[78:81]
	v_mfma_f32_16x16x32_bf16 v[70:73], v[146:149], v[204:207], v[70:73]
	s_setprio 0
	s_setprio 1
	v_mfma_f32_16x16x32_bf16 v[138:141], v[150:153], v[166:169], v[138:141]
	v_mfma_f32_16x16x32_bf16 v[130:133], v[158:161], v[166:169], v[130:133]
	v_mfma_f32_16x16x32_bf16 v[114:117], v[150:153], v[174:177], v[114:117]
	v_mfma_f32_16x16x32_bf16 v[110:113], v[158:161], v[174:177], v[110:113]
	v_mfma_f32_16x16x32_bf16 v[86:89], v[150:153], v[184:187], v[86:89]
	v_mfma_f32_16x16x32_bf16 v[82:85], v[158:161], v[184:187], v[82:85]
	v_mfma_f32_16x16x32_bf16 v[62:65], v[150:153], v[200:203], v[62:65]
	v_mfma_f32_16x16x32_bf16 v[54:57], v[158:161], v[200:203], v[54:57]
	v_mfma_f32_16x16x32_bf16 v[138:141], v[154:157], v[170:173], v[138:141]
	v_mfma_f32_16x16x32_bf16 v[130:133], v[162:165], v[170:173], v[130:133]
	v_mfma_f32_16x16x32_bf16 v[114:117], v[154:157], v[178:181], v[114:117]
	v_mfma_f32_16x16x32_bf16 v[110:113], v[162:165], v[178:181], v[110:113]
	v_mfma_f32_16x16x32_bf16 v[86:89], v[154:157], v[194:197], v[86:89]
	v_mfma_f32_16x16x32_bf16 v[82:85], v[162:165], v[194:197], v[82:85]
	v_mfma_f32_16x16x32_bf16 v[62:65], v[154:157], v[204:207], v[62:65]
	v_mfma_f32_16x16x32_bf16 v[54:57], v[162:165], v[204:207], v[54:57]
	s_setprio 0
	s_barrier
;     ...
;         PG8_TRIP(0, true);
; #pragma unroll 1
;         for (int t = 2; t < nt; t += 2) PG8_TRIP(t, false);
	s_add_u32 s18, s44, 0x80
	s_addc_u32 s19, s45, 0
	s_mov_b32 m0, s61
	ds_read_b128 v[166:169], v199 offset:49152
	ds_read_b128 v[170:173], v199 offset:50176
	ds_read_b128 v[174:177], v199 offset:51200
	ds_read_b128 v[178:181], v199 offset:52224
	ds_read_b128 v[184:187], v199 offset:53248
	ds_read_b128 v[194:197], v199 offset:54272
	ds_read_b128 v[200:203], v199 offset:55296
	ds_read_b128 v[204:207], v199 offset:56320
	s_nop 0
	v_lshl_add_u64 v[188:189], s[18:19], 0, v[190:191]
	global_load_lds_dwordx4 v[188:189], off
	v_lshl_add_u64 v[188:189], s[18:19], 0, v[182:183]
	s_add_u32 s18, s44, 0x40080
	s_mov_b32 m0, s62
	s_addc_u32 s19, s45, 0
	global_load_lds_dwordx4 v[188:189], off
	s_mov_b32 m0, s63
	v_lshl_add_u64 v[188:189], s[18:19], 0, v[190:191]
	global_load_lds_dwordx4 v[188:189], off
	v_lshl_add_u64 v[188:189], s[18:19], 0, v[182:183]
	s_mov_b32 m0, s64
	s_nop 0
	global_load_lds_dwordx4 v[188:189], off
	s_mov_b32 m0, s53
	v_lshl_add_u64 v[188:189], s[42:43], 0, v[190:191]
	global_load_lds_dwordx4 v[188:189], off
	v_lshl_add_u64 v[188:189], s[42:43], 0, v[182:183]
	s_mov_b32 m0, s54
	s_nop 0
	global_load_lds_dwordx4 v[188:189], off
	s_waitcnt vmcnt(8)
	s_waitcnt lgkmcnt(0)
	s_barrier
	s_setprio 1
	s_waitcnt lgkmcnt(0)
	v_mfma_f32_16x16x32_bf16 v[74:77], v[102:105], v[166:169], v[74:77]
	v_mfma_f32_16x16x32_bf16 v[66:69], v[118:121], v[166:169], v[66:69]
	v_mfma_f32_16x16x32_bf16 v[46:49], v[102:105], v[174:177], v[46:49]
	v_mfma_f32_16x16x32_bf16 v[42:45], v[118:121], v[174:177], v[42:45]
	v_mfma_f32_16x16x32_bf16 v[30:33], v[102:105], v[184:187], v[30:33]
	v_mfma_f32_16x16x32_bf16 v[26:29], v[118:121], v[184:187], v[26:29]
	v_mfma_f32_16x16x32_bf16 v[14:17], v[102:105], v[200:203], v[14:17]
	v_mfma_f32_16x16x32_bf16 v[10:13], v[118:121], v[200:203], v[10:13]
	v_mfma_f32_16x16x32_bf16 v[74:77], v[106:109], v[170:173], v[74:77]
	v_mfma_f32_16x16x32_bf16 v[66:69], v[146:149], v[170:173], v[66:69]
	v_mfma_f32_16x16x32_bf16 v[46:49], v[106:109], v[178:181], v[46:49]
	v_mfma_f32_16x16x32_bf16 v[42:45], v[146:149], v[178:181], v[42:45]
	v_mfma_f32_16x16x32_bf16 v[30:33], v[106:109], v[194:197], v[30:33]
	v_mfma_f32_16x16x32_bf16 v[26:29], v[146:149], v[194:197], v[26:29]
	v_mfma_f32_16x16x32_bf16 v[14:17], v[106:109], v[204:207], v[14:17]
	v_mfma_f32_16x16x32_bf16 v[10:13], v[146:149], v[204:207], v[10:13]
	s_setprio 0
	s_setprio 1
	v_mfma_f32_16x16x32_bf16 v[58:61], v[150:153], v[166:169], v[58:61]
	v_mfma_f32_16x16x32_bf16 v[50:53], v[158:161], v[166:169], v[50:53]
	v_mfma_f32_16x16x32_bf16 v[38:41], v[150:153], v[174:177], v[38:41]
	v_mfma_f32_16x16x32_bf16 v[34:37], v[158:161], v[174:177], v[34:37]
	v_mfma_f32_16x16x32_bf16 v[22:25], v[150:153], v[184:187], v[22:25]
	v_mfma_f32_16x16x32_bf16 v[18:21], v[158:161], v[184:187], v[18:21]
	v_mfma_f32_16x16x32_bf16 v[6:9], v[150:153], v[200:203], v[6:9]
	v_mfma_f32_16x16x32_bf16 v[2:5], v[158:161], v[200:203], v[2:5]
	v_mfma_f32_16x16x32_bf16 v[58:61], v[154:157], v[170:173], v[58:61]
	v_mfma_f32_16x16x32_bf16 v[50:53], v[162:165], v[170:173], v[50:53]
	v_mfma_f32_16x16x32_bf16 v[38:41], v[154:157], v[178:181], v[38:41]
	v_mfma_f32_16x16x32_bf16 v[34:37], v[162:165], v[178:181], v[34:37]
	v_mfma_f32_16x16x32_bf16 v[22:25], v[154:157], v[194:197], v[22:25]
	v_mfma_f32_16x16x32_bf16 v[18:21], v[162:165], v[194:197], v[18:21]
	v_mfma_f32_16x16x32_bf16 v[6:9], v[154:157], v[204:207], v[6:9]
	v_mfma_f32_16x16x32_bf16 v[2:5], v[162:165], v[204:207], v[2:5]
	s_add_i32 s65, s65, 2
	s_cmp_gt_u32 s65, 13
	s_mov_b64 s[38:39], s[40:41]
	s_setprio 0
	s_barrier
	s_cbranch_scc0 .LBB0_1064
	s_and_b64 vcc, exec, s[2:3]
	s_cbranch_vccz .LBB0_1067
	s_barrier

.LBB0_1082:
	s_cmp_eq_u32 s64, 4
	s_cselect_b64 s[40:41], -1, 0
	s_and_b64 s[42:43], s[36:37], s[40:41]
	s_and_b64 s[40:41], s[42:43], exec
	s_cselect_b32 s44, s35, s29
	s_cselect_b32 s45, s34, s28
	s_add_u32 s40, s30, 0x100
	ds_read_b128 v[18:21], v162
	ds_read_b128 v[22:25], v162 offset:1024
	ds_read_b128 v[26:29], v162 offset:2048
	ds_read_b128 v[30:33], v162 offset:3072
	ds_read_b128 v[10:13], v163
	ds_read_b128 v[14:17], v163 offset:1024
	ds_read_b128 v[2:5], v163 offset:2048
	ds_read_b128 v[6:9], v163 offset:3072
	s_addc_u32 s41, s31, 0
	s_and_b32 s65, s40, 0x300
	s_add_u32 s48, s45, s65
	s_addc_u32 s49, s44, 0
	s_and_b64 s[42:43], s[42:43], exec
	s_cselect_b32 s45, s39, s9
	s_cselect_b32 s44, s38, s8
	s_add_u32 s42, s48, 0x80
	s_addc_u32 s43, s49, 0
	s_add_u32 s44, s44, s65
	s_addc_u32 s45, s45, 0
	s_add_u32 s30, s28, s30
	s_addc_u32 s31, s29, s31
	s_add_u32 s30, s30, 0x20080
	s_addc_u32 s31, s31, 0
	s_mov_b32 m0, s3
	ds_read_b128 v[166:169], v215
	ds_read_b128 v[170:173], v215 offset:1024
	ds_read_b128 v[180:183], v215 offset:2048
	ds_read_b128 v[184:187], v215 offset:3072
	ds_read_b128 v[194:197], v215 offset:4096
	ds_read_b128 v[198:201], v215 offset:5120
	ds_read_b128 v[216:219], v215 offset:6144
	ds_read_b128 v[220:223], v215 offset:7168
	s_nop 0
	v_lshl_add_u64 v[174:175], s[30:31], 0, v[190:191]
	global_load_lds_dwordx4 v[174:175], off
	v_lshl_add_u64 v[174:175], s[30:31], 0, v[178:179]
	s_mov_b32 m0, s11
	s_nop 0
	global_load_lds_dwordx4 v[174:175], off
	s_waitcnt vmcnt(8)
	s_waitcnt lgkmcnt(0)
	s_barrier
	s_setprio 1
	s_waitcnt lgkmcnt(0)
	v_mfma_f32_16x16x128_f8f6f4 v[146:149], v[18:25], v[166:173], v[146:149]
	v_mfma_f32_16x16x128_f8f6f4 v[150:153], v[26:33], v[166:173], v[150:153]
	v_mfma_f32_16x16x128_f8f6f4 v[138:141], v[18:25], v[180:187], v[138:141]
	v_mfma_f32_16x16x128_f8f6f4 v[130:133], v[26:33], v[180:187], v[130:133]
	v_mfma_f32_16x16x128_f8f6f4 v[126:129], v[18:25], v[194:201], v[126:129]
	v_mfma_f32_16x16x128_f8f6f4 v[118:121], v[26:33], v[194:201], v[118:121]
	v_mfma_f32_16x16x128_f8f6f4 v[106:109], v[18:25], v[216:223], v[106:109]
	v_mfma_f32_16x16x128_f8f6f4 v[94:97], v[26:33], v[216:223], v[94:97]
	s_setprio 0
	s_setprio 1
	v_mfma_f32_16x16x128_f8f6f4 v[154:157], v[10:17], v[166:173], v[154:157]
	v_mfma_f32_16x16x128_f8f6f4 v[158:161], v[2:9], v[166:173], v[158:161]
	v_mfma_f32_16x16x128_f8f6f4 v[142:145], v[10:17], v[180:187], v[142:145]
	v_mfma_f32_16x16x128_f8f6f4 v[134:137], v[2:9], v[180:187], v[134:137]
	v_mfma_f32_16x16x128_f8f6f4 v[122:125], v[10:17], v[194:201], v[122:125]
	v_mfma_f32_16x16x128_f8f6f4 v[114:117], v[2:9], v[194:201], v[114:117]
	v_mfma_f32_16x16x128_f8f6f4 v[86:89], v[10:17], v[216:223], v[86:89]
	v_mfma_f32_16x16x128_f8f6f4 v[82:85], v[2:9], v[216:223], v[82:85]
	s_setprio 0
	s_barrier
	s_mov_b64 s[30:31], s[44:45]
	s_mov_b32 m0, s23
	ds_read_b128 v[166:169], v215 offset:16384
	ds_read_b128 v[170:173], v215 offset:17408
	ds_read_b128 v[180:183], v215 offset:18432
	ds_read_b128 v[184:187], v215 offset:19456
	ds_read_b128 v[194:197], v215 offset:20480
	ds_read_b128 v[198:201], v215 offset:21504
	ds_read_b128 v[216:219], v215 offset:22528
	ds_read_b128 v[220:223], v215 offset:23552
	s_nop 0
	v_lshl_add_u64 v[174:175], s[30:31], 0, v[190:191]
	global_load_lds_dwordx4 v[174:175], off
	v_lshl_add_u64 v[174:175], s[30:31], 0, v[178:179]
	s_add_u32 s30, s44, 0x20000
	s_mov_b32 m0, s58
	s_addc_u32 s31, s45, 0
	global_load_lds_dwordx4 v[174:175], off
	s_mov_b32 m0, s59
	v_lshl_add_u64 v[174:175], s[30:31], 0, v[190:191]
	global_load_lds_dwordx4 v[174:175], off
	v_lshl_add_u64 v[174:175], s[30:31], 0, v[178:179]
	s_mov_b32 m0, s61
	s_mov_b64 s[30:31], s[48:49]
	global_load_lds_dwordx4 v[174:175], off
	s_mov_b32 m0, s7
	v_lshl_add_u64 v[174:175], s[30:31], 0, v[190:191]
	global_load_lds_dwordx4 v[174:175], off
	v_lshl_add_u64 v[174:175], s[30:31], 0, v[178:179]
	s_mov_b32 m0, s52
	s_nop 0
	global_load_lds_dwordx4 v[174:175], off
	s_waitcnt vmcnt(8)
	s_waitcnt lgkmcnt(0)
	s_barrier
	s_setprio 1
	s_waitcnt lgkmcnt(0)
	v_mfma_f32_16x16x128_f8f6f4 v[110:113], v[18:25], v[166:173], v[110:113]
	v_mfma_f32_16x16x128_f8f6f4 v[98:101], v[26:33], v[166:173], v[98:101]
	v_mfma_f32_16x16x128_f8f6f4 v[78:81], v[18:25], v[180:187], v[78:81]
	v_mfma_f32_16x16x128_f8f6f4 v[74:77], v[26:33], v[180:187], v[74:77]
	v_mfma_f32_16x16x128_f8f6f4 v[62:65], v[18:25], v[194:201], v[62:65]
	v_mfma_f32_16x16x128_f8f6f4 v[58:61], v[26:33], v[194:201], v[58:61]
	v_mfma_f32_16x16x128_f8f6f4 v[46:49], v[18:25], v[216:223], v[46:49]
	v_mfma_f32_16x16x128_f8f6f4 v[42:45], v[26:33], v[216:223], v[42:45]
	s_setprio 0
	s_setprio 1
	v_mfma_f32_16x16x128_f8f6f4 v[102:105], v[10:17], v[166:173], v[102:105]
	v_mfma_f32_16x16x128_f8f6f4 v[90:93], v[2:9], v[166:173], v[90:93]
	v_mfma_f32_16x16x128_f8f6f4 v[70:73], v[10:17], v[180:187], v[70:73]
	v_mfma_f32_16x16x128_f8f6f4 v[66:69], v[2:9], v[180:187], v[66:69]
	v_mfma_f32_16x16x128_f8f6f4 v[54:57], v[10:17], v[194:201], v[54:57]
	v_mfma_f32_16x16x128_f8f6f4 v[50:53], v[2:9], v[194:201], v[50:53]
	v_mfma_f32_16x16x128_f8f6f4 v[38:41], v[10:17], v[216:223], v[38:41]
	v_mfma_f32_16x16x128_f8f6f4 v[34:37], v[2:9], v[216:223], v[34:37]
	s_setprio 0
	s_barrier
;     ...
;         PG8_TRIP(0, true);
; #pragma unroll 1
;         for (int t = 2; t < nt; t += 2) PG8_TRIP(t, false);
	ds_read_b128 v[26:29], v164
	ds_read_b128 v[30:33], v164 offset:1024
	ds_read_b128 v[18:21], v164 offset:2048
	ds_read_b128 v[22:25], v164 offset:3072
	ds_read_b128 v[10:13], v165
	ds_read_b128 v[14:17], v165 offset:1024
	ds_read_b128 v[2:5], v165 offset:2048
	ds_read_b128 v[6:9], v165 offset:3072
	s_add_u32 s30, s48, 0x20000
	s_addc_u32 s31, s49, 0
	s_mov_b32 m0, s53
	ds_read_b128 v[166:169], v215 offset:32768
	ds_read_b128 v[170:173], v215 offset:33792
	ds_read_b128 v[180:183], v215 offset:34816
	ds_read_b128 v[184:187], v215 offset:35840
	ds_read_b128 v[194:197], v215 offset:36864
	ds_read_b128 v[198:201], v215 offset:37888
	ds_read_b128 v[216:219], v215 offset:38912
	ds_read_b128 v[220:223], v215 offset:39936
	s_nop 0
	v_lshl_add_u64 v[174:175], s[30:31], 0, v[190:191]
	global_load_lds_dwordx4 v[174:175], off
	v_lshl_add_u64 v[174:175], s[30:31], 0, v[178:179]
	s_mov_b32 m0, s54
	s_nop 0
	global_load_lds_dwordx4 v[174:175], off
	s_waitcnt vmcnt(8)
	s_waitcnt lgkmcnt(0)
	s_barrier
	s_setprio 1
	s_waitcnt lgkmcnt(0)
	v_mfma_f32_16x16x128_f8f6f4 v[146:149], v[26:33], v[166:173], v[146:149]
	v_mfma_f32_16x16x128_f8f6f4 v[150:153], v[18:25], v[166:173], v[150:153]
	v_mfma_f32_16x16x128_f8f6f4 v[138:141], v[26:33], v[180:187], v[138:141]
	v_mfma_f32_16x16x128_f8f6f4 v[130:133], v[18:25], v[180:187], v[130:133]
	v_mfma_f32_16x16x128_f8f6f4 v[126:129], v[26:33], v[194:201], v[126:129]
	v_mfma_f32_16x16x128_f8f6f4 v[118:121], v[18:25], v[194:201], v[118:121]
	v_mfma_f32_16x16x128_f8f6f4 v[106:109], v[26:33], v[216:223], v[106:109]
	v_mfma_f32_16x16x128_f8f6f4 v[94:97], v[18:25], v[216:223], v[94:97]
	s_setprio 0
	s_setprio 1
	v_mfma_f32_16x16x128_f8f6f4 v[154:157], v[10:17], v[166:173], v[154:157]
	v_mfma_f32_16x16x128_f8f6f4 v[158:161], v[2:9], v[166:173], v[158:161]
	v_mfma_f32_16x16x128_f8f6f4 v[142:145], v[10:17], v[180:187], v[142:145]
	v_mfma_f32_16x16x128_f8f6f4 v[134:137], v[2:9], v[180:187], v[134:137]
	v_mfma_f32_16x16x128_f8f6f4 v[122:125], v[10:17], v[194:201], v[122:125]
	v_mfma_f32_16x16x128_f8f6f4 v[114:117], v[2:9], v[194:201], v[114:117]
	v_mfma_f32_16x16x128_f8f6f4 v[86:89], v[10:17], v[216:223], v[86:89]
	v_mfma_f32_16x16x128_f8f6f4 v[82:85], v[2:9], v[216:223], v[82:85]
	s_setprio 0
	s_barrier
	s_add_u32 s30, s44, 0x80
	s_addc_u32 s31, s45, 0
	s_mov_b32 m0, s18
	ds_read_b128 v[166:169], v215 offset:49152
	ds_read_b128 v[170:173], v215 offset:50176
	ds_read_b128 v[180:183], v215 offset:51200
	ds_read_b128 v[184:187], v215 offset:52224
	ds_read_b128 v[194:197], v215 offset:53248
	ds_read_b128 v[198:201], v215 offset:54272
	ds_read_b128 v[216:219], v215 offset:55296
	ds_read_b128 v[220:223], v215 offset:56320
	s_nop 0
	v_lshl_add_u64 v[174:175], s[30:31], 0, v[190:191]
	global_load_lds_dwordx4 v[174:175], off
	v_lshl_add_u64 v[174:175], s[30:31], 0, v[178:179]
	s_add_u32 s30, s44, 0x20080
	s_mov_b32 m0, s19
	s_addc_u32 s31, s45, 0
	global_load_lds_dwordx4 v[174:175], off
	s_mov_b32 m0, s62
	v_lshl_add_u64 v[174:175], s[30:31], 0, v[190:191]
	global_load_lds_dwordx4 v[174:175], off
	v_lshl_add_u64 v[174:175], s[30:31], 0, v[178:179]
	s_mov_b32 m0, s63
	s_nop 0
	global_load_lds_dwordx4 v[174:175], off
	s_mov_b32 m0, s55
	v_lshl_add_u64 v[174:175], s[42:43], 0, v[190:191]
	global_load_lds_dwordx4 v[174:175], off
	v_lshl_add_u64 v[174:175], s[42:43], 0, v[178:179]
	s_mov_b32 m0, s56
	s_nop 0
	global_load_lds_dwordx4 v[174:175], off
	s_waitcnt vmcnt(8)
	s_waitcnt lgkmcnt(0)
	s_barrier
	s_setprio 1
	s_waitcnt lgkmcnt(0)
	v_mfma_f32_16x16x128_f8f6f4 v[110:113], v[26:33], v[166:173], v[110:113]
	v_mfma_f32_16x16x128_f8f6f4 v[98:101], v[18:25], v[166:173], v[98:101]
	v_mfma_f32_16x16x128_f8f6f4 v[78:81], v[26:33], v[180:187], v[78:81]
	v_mfma_f32_16x16x128_f8f6f4 v[74:77], v[18:25], v[180:187], v[74:77]
	v_mfma_f32_16x16x128_f8f6f4 v[62:65], v[26:33], v[194:201], v[62:65]
	v_mfma_f32_16x16x128_f8f6f4 v[58:61], v[18:25], v[194:201], v[58:61]
	v_mfma_f32_16x16x128_f8f6f4 v[46:49], v[26:33], v[216:223], v[46:49]
	v_mfma_f32_16x16x128_f8f6f4 v[42:45], v[18:25], v[216:223], v[42:45]
	s_setprio 0
	s_setprio 1
	v_mfma_f32_16x16x128_f8f6f4 v[102:105], v[10:17], v[166:173], v[102:105]
	v_mfma_f32_16x16x128_f8f6f4 v[90:93], v[2:9], v[166:173], v[90:93]
	v_mfma_f32_16x16x128_f8f6f4 v[70:73], v[10:17], v[180:187], v[70:73]
	v_mfma_f32_16x16x128_f8f6f4 v[66:69], v[2:9], v[180:187], v[66:69]
	v_mfma_f32_16x16x128_f8f6f4 v[54:57], v[10:17], v[194:201], v[54:57]
	v_mfma_f32_16x16x128_f8f6f4 v[50:53], v[2:9], v[194:201], v[50:53]
	v_mfma_f32_16x16x128_f8f6f4 v[38:41], v[10:17], v[216:223], v[38:41]
	v_mfma_f32_16x16x128_f8f6f4 v[34:37], v[2:9], v[216:223], v[34:37]
	s_add_i32 s64, s64, 2
	s_cmp_gt_u32 s64, 5
	s_mov_b64 s[30:31], s[40:41]
	s_setprio 0
	s_barrier
	s_cbranch_scc0 .LBB0_1082
	s_and_b64 vcc, exec, s[4:5]
	s_cbranch_vccz .LBB0_1085
	s_barrier

.LBB0_1424:
	s_cmp_eq_u32 s59, 4
	s_cselect_b64 vcc, -1, 0
	s_add_u32 s60, s82, s28
	ds_read_b128 v[18:21], v181
	ds_read_b128 v[22:25], v181 offset:1024
	ds_read_b128 v[26:29], v181 offset:2048
	ds_read_b128 v[30:33], v181 offset:3072
	ds_read_b128 v[10:13], v182
	ds_read_b128 v[14:17], v182 offset:1024
	ds_read_b128 v[2:5], v182 offset:2048
	ds_read_b128 v[6:9], v182 offset:3072
	s_addc_u32 s61, s83, s29
	s_add_i32 s30, s28, 0xe4d00100
	s_and_b32 s34, s30, 0x300
	s_add_u32 s38, s96, s34
	s_addc_u32 s39, s97, 0
	s_and_b64 s[30:31], s[22:23], vcc
	s_and_b64 s[30:31], s[30:31], exec
	s_cselect_b32 s35, s9, s11
	s_cselect_b32 s62, s8, s10
	s_add_u32 s30, s38, 0x80
	s_addc_u32 s31, s39, 0
	s_add_u32 s34, s62, s34
	s_addc_u32 s35, s35, 0
	s_add_u32 s60, s60, 0x80
	v_cndmask_b32_e32 v185, v170, v177, vcc
	v_cndmask_b32_e32 v188, v168, v178, vcc
	v_cndmask_b32_e32 v189, v190, v179, vcc
	v_cndmask_b32_e32 v193, v166, v180, vcc
	s_addc_u32 s61, s61, 0
	s_mov_b32 m0, s7
	ds_read_b128 v[194:197], v171
	ds_read_b128 v[198:201], v171 offset:1024
	ds_read_b128 v[214:217], v171 offset:2048
	ds_read_b128 v[218:221], v171 offset:3072
	ds_read_b128 v[222:225], v171 offset:4096
	ds_read_b128 v[226:229], v171 offset:5120
	ds_read_b128 v[230:233], v171 offset:6144
	ds_read_b128 v[234:237], v171 offset:7168
	s_nop 0
	v_lshl_add_u64 v[186:187], s[60:61], 0, v[190:191]
	global_load_lds_dwordx4 v[186:187], off
	v_lshl_add_u64 v[186:187], s[60:61], 0, v[166:167]
	s_mov_b32 m0, s52
	s_nop 0
	global_load_lds_dwordx4 v[186:187], off
	s_waitcnt vmcnt(8)
	s_waitcnt lgkmcnt(0)
	s_barrier
	s_setprio 1
	s_waitcnt lgkmcnt(0)
	v_mfma_f32_16x16x128_f8f6f4 v[150:153], v[18:25], v[194:201], v[150:153]
	v_mfma_f32_16x16x128_f8f6f4 v[146:149], v[26:33], v[194:201], v[146:149]
	v_mfma_f32_16x16x128_f8f6f4 v[134:137], v[18:25], v[214:221], v[134:137]
	v_mfma_f32_16x16x128_f8f6f4 v[130:133], v[26:33], v[214:221], v[130:133]
	v_mfma_f32_16x16x128_f8f6f4 v[118:121], v[18:25], v[222:229], v[118:121]
	v_mfma_f32_16x16x128_f8f6f4 v[114:117], v[26:33], v[222:229], v[114:117]
	v_mfma_f32_16x16x128_f8f6f4 v[90:93], v[18:25], v[230:237], v[90:93]
	v_mfma_f32_16x16x128_f8f6f4 v[82:85], v[26:33], v[230:237], v[82:85]
	s_setprio 0
	s_setprio 1
	v_mfma_f32_16x16x128_f8f6f4 v[158:161], v[10:17], v[194:201], v[158:161]
	v_mfma_f32_16x16x128_f8f6f4 v[154:157], v[2:9], v[194:201], v[154:157]
	v_mfma_f32_16x16x128_f8f6f4 v[142:145], v[10:17], v[214:221], v[142:145]
	v_mfma_f32_16x16x128_f8f6f4 v[138:141], v[2:9], v[214:221], v[138:141]
	v_mfma_f32_16x16x128_f8f6f4 v[126:129], v[10:17], v[222:229], v[126:129]
	v_mfma_f32_16x16x128_f8f6f4 v[122:125], v[2:9], v[222:229], v[122:125]
	v_mfma_f32_16x16x128_f8f6f4 v[102:105], v[10:17], v[230:237], v[102:105]
	v_mfma_f32_16x16x128_f8f6f4 v[98:101], v[2:9], v[230:237], v[98:101]
	s_setprio 0
	s_barrier
	s_mov_b64 s[60:61], s[34:35]
	s_mov_b32 m0, s53
	ds_read_b128 v[194:197], v171 offset:16384
	ds_read_b128 v[198:201], v171 offset:17408
	ds_read_b128 v[214:217], v171 offset:18432
	ds_read_b128 v[218:221], v171 offset:19456
	ds_read_b128 v[222:225], v171 offset:20480
	ds_read_b128 v[226:229], v171 offset:21504
	ds_read_b128 v[230:233], v171 offset:22528
	ds_read_b128 v[234:237], v171 offset:23552
	s_nop 0
	v_lshl_add_u64 v[186:187], s[60:61], 0, v[164:165]
	global_load_lds_dwordx4 v[186:187], off
	v_lshl_add_u64 v[186:187], s[60:61], 0, v[162:163]
	s_add_u32 s60, s34, 0x20000
	s_mov_b32 m0, s18
	s_addc_u32 s61, s35, 0
	global_load_lds_dwordx4 v[186:187], off
	s_mov_b32 m0, s19
	v_lshl_add_u64 v[186:187], s[60:61], 0, v[164:165]
	global_load_lds_dwordx4 v[186:187], off
	v_lshl_add_u64 v[186:187], s[60:61], 0, v[162:163]
	s_mov_b32 m0, s54
	s_mov_b64 s[60:61], s[38:39]
	global_load_lds_dwordx4 v[186:187], off
	s_mov_b32 m0, s40
	s_nop 0
	global_load_lds_dwordx4 v185, s[60:61]
	s_mov_b32 m0, s41
	s_nop 0
	global_load_lds_dwordx4 v188, s[60:61]
	s_waitcnt vmcnt(8)
	s_waitcnt lgkmcnt(0)
	s_barrier
	s_setprio 1
	s_waitcnt lgkmcnt(0)
	v_mfma_f32_16x16x128_f8f6f4 v[94:97], v[18:25], v[194:201], v[94:97]
	v_mfma_f32_16x16x128_f8f6f4 v[86:89], v[26:33], v[194:201], v[86:89]
	v_mfma_f32_16x16x128_f8f6f4 v[70:73], v[18:25], v[214:221], v[70:73]
	v_mfma_f32_16x16x128_f8f6f4 v[66:69], v[26:33], v[214:221], v[66:69]
	v_mfma_f32_16x16x128_f8f6f4 v[54:57], v[18:25], v[222:229], v[54:57]
	v_mfma_f32_16x16x128_f8f6f4 v[50:53], v[26:33], v[222:229], v[50:53]
	v_mfma_f32_16x16x128_f8f6f4 v[38:41], v[18:25], v[230:237], v[38:41]
	v_mfma_f32_16x16x128_f8f6f4 v[34:37], v[26:33], v[230:237], v[34:37]
	s_setprio 0
	s_setprio 1
	v_mfma_f32_16x16x128_f8f6f4 v[110:113], v[10:17], v[194:201], v[110:113]
	v_mfma_f32_16x16x128_f8f6f4 v[106:109], v[2:9], v[194:201], v[106:109]
	v_mfma_f32_16x16x128_f8f6f4 v[78:81], v[10:17], v[214:221], v[78:81]
	v_mfma_f32_16x16x128_f8f6f4 v[74:77], v[2:9], v[214:221], v[74:77]
	v_mfma_f32_16x16x128_f8f6f4 v[62:65], v[10:17], v[222:229], v[62:65]
	v_mfma_f32_16x16x128_f8f6f4 v[58:61], v[2:9], v[222:229], v[58:61]
	v_mfma_f32_16x16x128_f8f6f4 v[46:49], v[10:17], v[230:237], v[46:49]
	v_mfma_f32_16x16x128_f8f6f4 v[42:45], v[2:9], v[230:237], v[42:45]
	s_setprio 0
	s_barrier
;     ...
;         PG8_TRIP(0, true);
; #pragma unroll 1
;         for (int t = 2; t < nt; t += 2) PG8_TRIP(t, false);
	ds_read_b128 v[26:29], v183
	ds_read_b128 v[30:33], v183 offset:1024
	ds_read_b128 v[18:21], v183 offset:2048
	ds_read_b128 v[22:25], v183 offset:3072
	ds_read_b128 v[10:13], v184
	ds_read_b128 v[14:17], v184 offset:1024
	ds_read_b128 v[2:5], v184 offset:2048
	ds_read_b128 v[6:9], v184 offset:3072
	s_mov_b32 m0, s42
	ds_read_b128 v[194:197], v171 offset:32768
	ds_read_b128 v[198:201], v171 offset:33792
	ds_read_b128 v[214:217], v171 offset:34816
	ds_read_b128 v[218:221], v171 offset:35840
	ds_read_b128 v[222:225], v171 offset:36864
	ds_read_b128 v[226:229], v171 offset:37888
	ds_read_b128 v[230:233], v171 offset:38912
	ds_read_b128 v[234:237], v171 offset:39936
	s_nop 0
	global_load_lds_dwordx4 v189, s[38:39]
	s_mov_b32 m0, s43
	s_nop 0
	global_load_lds_dwordx4 v193, s[38:39]
	s_waitcnt vmcnt(8)
	s_waitcnt lgkmcnt(0)
	s_barrier
	s_setprio 1
	s_waitcnt lgkmcnt(0)
	v_mfma_f32_16x16x128_f8f6f4 v[150:153], v[26:33], v[194:201], v[150:153]
	v_mfma_f32_16x16x128_f8f6f4 v[146:149], v[18:25], v[194:201], v[146:149]
	v_mfma_f32_16x16x128_f8f6f4 v[134:137], v[26:33], v[214:221], v[134:137]
	v_mfma_f32_16x16x128_f8f6f4 v[130:133], v[18:25], v[214:221], v[130:133]
	v_mfma_f32_16x16x128_f8f6f4 v[118:121], v[26:33], v[222:229], v[118:121]
	v_mfma_f32_16x16x128_f8f6f4 v[114:117], v[18:25], v[222:229], v[114:117]
	v_mfma_f32_16x16x128_f8f6f4 v[90:93], v[26:33], v[230:237], v[90:93]
	v_mfma_f32_16x16x128_f8f6f4 v[82:85], v[18:25], v[230:237], v[82:85]
	s_setprio 0
	s_setprio 1
	v_mfma_f32_16x16x128_f8f6f4 v[158:161], v[10:17], v[194:201], v[158:161]
	v_mfma_f32_16x16x128_f8f6f4 v[154:157], v[2:9], v[194:201], v[154:157]
	v_mfma_f32_16x16x128_f8f6f4 v[142:145], v[10:17], v[214:221], v[142:145]
	v_mfma_f32_16x16x128_f8f6f4 v[138:141], v[2:9], v[214:221], v[138:141]
	v_mfma_f32_16x16x128_f8f6f4 v[126:129], v[10:17], v[222:229], v[126:129]
	v_mfma_f32_16x16x128_f8f6f4 v[122:125], v[2:9], v[222:229], v[122:125]
	v_mfma_f32_16x16x128_f8f6f4 v[102:105], v[10:17], v[230:237], v[102:105]
	v_mfma_f32_16x16x128_f8f6f4 v[98:101], v[2:9], v[230:237], v[98:101]
	s_setprio 0
	s_barrier
	s_add_u32 s38, s34, 0x80
	s_addc_u32 s39, s35, 0
	s_mov_b32 m0, s55
	ds_read_b128 v[194:197], v171 offset:49152
	ds_read_b128 v[198:201], v171 offset:50176
	ds_read_b128 v[214:217], v171 offset:51200
	ds_read_b128 v[218:221], v171 offset:52224
	ds_read_b128 v[222:225], v171 offset:53248
	ds_read_b128 v[226:229], v171 offset:54272
	ds_read_b128 v[230:233], v171 offset:55296
	ds_read_b128 v[234:237], v171 offset:56320
	s_add_u32 s34, s34, 0x20080
	v_lshl_add_u64 v[186:187], s[38:39], 0, v[164:165]
	global_load_lds_dwordx4 v[186:187], off
	v_lshl_add_u64 v[186:187], s[38:39], 0, v[162:163]
	s_mov_b32 m0, s56
	s_addc_u32 s35, s35, 0
	global_load_lds_dwordx4 v[186:187], off
	s_mov_b32 m0, s57
	v_lshl_add_u64 v[186:187], s[34:35], 0, v[164:165]
	global_load_lds_dwordx4 v[186:187], off
	v_lshl_add_u64 v[186:187], s[34:35], 0, v[162:163]
	s_mov_b32 m0, s58
	s_nop 0
	global_load_lds_dwordx4 v[186:187], off
	s_mov_b32 m0, s44
	s_nop 0
	global_load_lds_dwordx4 v185, s[30:31]
	s_mov_b32 m0, s45
	s_nop 0
	global_load_lds_dwordx4 v188, s[30:31]
	s_waitcnt vmcnt(8)
	s_waitcnt lgkmcnt(0)
	s_barrier
	s_setprio 1
	s_waitcnt lgkmcnt(0)
	v_mfma_f32_16x16x128_f8f6f4 v[94:97], v[26:33], v[194:201], v[94:97]
	v_mfma_f32_16x16x128_f8f6f4 v[86:89], v[18:25], v[194:201], v[86:89]
	v_mfma_f32_16x16x128_f8f6f4 v[70:73], v[26:33], v[214:221], v[70:73]
	v_mfma_f32_16x16x128_f8f6f4 v[66:69], v[18:25], v[214:221], v[66:69]
	v_mfma_f32_16x16x128_f8f6f4 v[54:57], v[26:33], v[222:229], v[54:57]
	v_mfma_f32_16x16x128_f8f6f4 v[50:53], v[18:25], v[222:229], v[50:53]
	v_mfma_f32_16x16x128_f8f6f4 v[38:41], v[26:33], v[230:237], v[38:41]
	v_mfma_f32_16x16x128_f8f6f4 v[34:37], v[18:25], v[230:237], v[34:37]
	s_setprio 0
	s_setprio 1
	v_mfma_f32_16x16x128_f8f6f4 v[110:113], v[10:17], v[194:201], v[110:113]
	v_mfma_f32_16x16x128_f8f6f4 v[106:109], v[2:9], v[194:201], v[106:109]
	v_mfma_f32_16x16x128_f8f6f4 v[78:81], v[10:17], v[214:221], v[78:81]
	v_mfma_f32_16x16x128_f8f6f4 v[74:77], v[2:9], v[214:221], v[74:77]
	v_mfma_f32_16x16x128_f8f6f4 v[62:65], v[10:17], v[222:229], v[62:65]
	v_mfma_f32_16x16x128_f8f6f4 v[58:61], v[2:9], v[222:229], v[58:61]
	v_mfma_f32_16x16x128_f8f6f4 v[46:49], v[10:17], v[230:237], v[46:49]
	v_mfma_f32_16x16x128_f8f6f4 v[42:45], v[2:9], v[230:237], v[42:45]
	s_add_i32 s59, s59, 2
	s_add_u32 s28, s28, 0x100
	s_addc_u32 s29, s29, 0
	s_cmp_gt_u32 s59, 5
	s_setprio 0
	s_barrier
	s_cbranch_scc0 .LBB0_1424
	s_and_b64 vcc, exec, s[2:3]
	s_cbranch_vccz .LBB0_1427
	s_barrier

.LBB0_1499:
	s_cmp_eq_u32 s61, 4
	s_cselect_b64 s[28:29], -1, 0
	s_and_b64 s[30:31], s[22:23], s[28:29]
	s_and_b64 s[28:29], s[30:31], exec
	s_cselect_b32 s40, s37, s7
	s_cselect_b32 s41, s36, s6
	s_add_u32 s28, s8, 0x100
	ds_read_b128 v[18:21], v166
	ds_read_b128 v[22:25], v166 offset:1024
	ds_read_b128 v[26:29], v166 offset:2048
	ds_read_b128 v[30:33], v166 offset:3072
	ds_read_b128 v[10:13], v167
	ds_read_b128 v[14:17], v167 offset:1024
	ds_read_b128 v[2:5], v167 offset:2048
	ds_read_b128 v[6:9], v167 offset:3072
	s_addc_u32 s29, s9, 0
	s_and_b32 s62, s28, 0x300
	s_add_u32 s42, s41, s62
	s_addc_u32 s43, s40, 0
	s_and_b64 s[30:31], s[30:31], exec
	s_cselect_b32 s41, s39, s3
	s_cselect_b32 s40, s38, s2
	s_add_u32 s30, s42, 0x80
	s_addc_u32 s31, s43, 0
	s_add_u32 s40, s40, s62
	s_addc_u32 s41, s41, 0
	s_add_u32 s8, s6, s8
	s_addc_u32 s9, s7, s9
	s_add_u32 s8, s8, 0x20080
	s_addc_u32 s9, s9, 0
	s_mov_b32 m0, s11
	ds_read_b128 v[174:177], v173
	ds_read_b128 v[178:181], v173 offset:1024
	ds_read_b128 v[182:185], v173 offset:2048
	ds_read_b128 v[186:189], v173 offset:3072
	ds_read_b128 v[194:197], v173 offset:4096
	ds_read_b128 v[198:201], v173 offset:5120
	ds_read_b128 v[214:217], v173 offset:6144
	ds_read_b128 v[218:221], v173 offset:7168
	s_nop 0
	v_lshl_add_u64 v[202:203], s[8:9], 0, v[164:165]
	global_load_lds_dwordx4 v[202:203], off
	v_lshl_add_u64 v[202:203], s[8:9], 0, v[162:163]
	s_mov_b32 m0, s35
	s_nop 0
	global_load_lds_dwordx4 v[202:203], off
	s_waitcnt vmcnt(8)
	s_waitcnt lgkmcnt(0)
	s_barrier
	s_setprio 1
	s_waitcnt lgkmcnt(0)
	v_mfma_f32_16x16x128_f8f6f4 v[154:157], v[18:25], v[174:181], v[154:157]
	v_mfma_f32_16x16x128_f8f6f4 v[158:161], v[26:33], v[174:181], v[158:161]
	v_mfma_f32_16x16x128_f8f6f4 v[138:141], v[18:25], v[182:189], v[138:141]
	v_mfma_f32_16x16x128_f8f6f4 v[130:133], v[26:33], v[182:189], v[130:133]
	v_mfma_f32_16x16x128_f8f6f4 v[126:129], v[18:25], v[194:201], v[126:129]
	v_mfma_f32_16x16x128_f8f6f4 v[122:125], v[26:33], v[194:201], v[122:125]
	v_mfma_f32_16x16x128_f8f6f4 v[110:113], v[18:25], v[214:221], v[110:113]
	v_mfma_f32_16x16x128_f8f6f4 v[106:109], v[26:33], v[214:221], v[106:109]
	s_setprio 0
	s_setprio 1
	v_mfma_f32_16x16x128_f8f6f4 v[146:149], v[10:17], v[174:181], v[146:149]
	v_mfma_f32_16x16x128_f8f6f4 v[150:153], v[2:9], v[174:181], v[150:153]
	v_mfma_f32_16x16x128_f8f6f4 v[142:145], v[10:17], v[182:189], v[142:145]
	v_mfma_f32_16x16x128_f8f6f4 v[134:137], v[2:9], v[182:189], v[134:137]
	v_mfma_f32_16x16x128_f8f6f4 v[118:121], v[10:17], v[194:201], v[118:121]
	v_mfma_f32_16x16x128_f8f6f4 v[114:117], v[2:9], v[194:201], v[114:117]
	v_mfma_f32_16x16x128_f8f6f4 v[94:97], v[10:17], v[214:221], v[94:97]
	v_mfma_f32_16x16x128_f8f6f4 v[90:93], v[2:9], v[214:221], v[90:93]
	s_setprio 0
	s_barrier
	s_mov_b64 s[8:9], s[40:41]
	s_mov_b32 m0, s55
	ds_read_b128 v[174:177], v173 offset:16384
	ds_read_b128 v[178:181], v173 offset:17408
	ds_read_b128 v[182:185], v173 offset:18432
	ds_read_b128 v[186:189], v173 offset:19456
	ds_read_b128 v[194:197], v173 offset:20480
	ds_read_b128 v[198:201], v173 offset:21504
	ds_read_b128 v[214:217], v173 offset:22528
	ds_read_b128 v[218:221], v173 offset:23552
	s_nop 0
	v_lshl_add_u64 v[202:203], s[8:9], 0, v[164:165]
	global_load_lds_dwordx4 v[202:203], off
	v_lshl_add_u64 v[202:203], s[8:9], 0, v[162:163]
	s_add_u32 s8, s40, 0x20000
	s_mov_b32 m0, s56
	s_addc_u32 s9, s41, 0
	global_load_lds_dwordx4 v[202:203], off
	s_mov_b32 m0, s57
	v_lshl_add_u64 v[202:203], s[8:9], 0, v[164:165]
	global_load_lds_dwordx4 v[202:203], off
	v_lshl_add_u64 v[202:203], s[8:9], 0, v[162:163]
	s_mov_b32 m0, s58
	s_mov_b64 s[8:9], s[42:43]
	global_load_lds_dwordx4 v[202:203], off
	s_mov_b32 m0, s44
	v_lshl_add_u64 v[202:203], s[8:9], 0, v[164:165]
	global_load_lds_dwordx4 v[202:203], off
	v_lshl_add_u64 v[202:203], s[8:9], 0, v[162:163]
	s_mov_b32 m0, s45
	s_nop 0
	global_load_lds_dwordx4 v[202:203], off
	s_waitcnt vmcnt(8)
	s_waitcnt lgkmcnt(0)
	s_barrier
	s_setprio 1
	s_waitcnt lgkmcnt(0)
	v_mfma_f32_16x16x128_f8f6f4 v[102:105], v[18:25], v[174:181], v[102:105]
	v_mfma_f32_16x16x128_f8f6f4 v[98:101], v[26:33], v[174:181], v[98:101]
	v_mfma_f32_16x16x128_f8f6f4 v[78:81], v[18:25], v[182:189], v[78:81]
	v_mfma_f32_16x16x128_f8f6f4 v[74:77], v[26:33], v[182:189], v[74:77]
	v_mfma_f32_16x16x128_f8f6f4 v[62:65], v[18:25], v[194:201], v[62:65]
	v_mfma_f32_16x16x128_f8f6f4 v[58:61], v[26:33], v[194:201], v[58:61]
	v_mfma_f32_16x16x128_f8f6f4 v[46:49], v[18:25], v[214:221], v[46:49]
	v_mfma_f32_16x16x128_f8f6f4 v[42:45], v[26:33], v[214:221], v[42:45]
	s_setprio 0
	s_setprio 1
	v_mfma_f32_16x16x128_f8f6f4 v[86:89], v[10:17], v[174:181], v[86:89]
	v_mfma_f32_16x16x128_f8f6f4 v[82:85], v[2:9], v[174:181], v[82:85]
	v_mfma_f32_16x16x128_f8f6f4 v[70:73], v[10:17], v[182:189], v[70:73]
	v_mfma_f32_16x16x128_f8f6f4 v[66:69], v[2:9], v[182:189], v[66:69]
	v_mfma_f32_16x16x128_f8f6f4 v[54:57], v[10:17], v[194:201], v[54:57]
	v_mfma_f32_16x16x128_f8f6f4 v[50:53], v[2:9], v[194:201], v[50:53]
	v_mfma_f32_16x16x128_f8f6f4 v[38:41], v[10:17], v[214:221], v[38:41]
	v_mfma_f32_16x16x128_f8f6f4 v[34:37], v[2:9], v[214:221], v[34:37]
	s_setprio 0
	s_barrier
;     ...
;         PG8_TRIP(0, true);
; #pragma unroll 1
;         for (int t = 2; t < nt; t += 2) PG8_TRIP(t, false);
	ds_read_b128 v[26:29], v168
	ds_read_b128 v[30:33], v168 offset:1024
	ds_read_b128 v[18:21], v168 offset:2048
	ds_read_b128 v[22:25], v168 offset:3072
	ds_read_b128 v[10:13], v170
	ds_read_b128 v[14:17], v170 offset:1024
	ds_read_b128 v[2:5], v170 offset:2048
	ds_read_b128 v[6:9], v170 offset:3072
	s_add_u32 s8, s42, 0x20000
	s_addc_u32 s9, s43, 0
	s_mov_b32 m0, s48
	ds_read_b128 v[174:177], v173 offset:32768
	ds_read_b128 v[178:181], v173 offset:33792
	ds_read_b128 v[182:185], v173 offset:34816
	ds_read_b128 v[186:189], v173 offset:35840
	ds_read_b128 v[194:197], v173 offset:36864
	ds_read_b128 v[198:201], v173 offset:37888
	ds_read_b128 v[214:217], v173 offset:38912
	ds_read_b128 v[218:221], v173 offset:39936
	s_nop 0
	v_lshl_add_u64 v[202:203], s[8:9], 0, v[164:165]
	global_load_lds_dwordx4 v[202:203], off
	v_lshl_add_u64 v[202:203], s[8:9], 0, v[162:163]
	s_mov_b32 m0, s49
	s_nop 0
	global_load_lds_dwordx4 v[202:203], off
	s_waitcnt vmcnt(8)
	s_waitcnt lgkmcnt(0)
	s_barrier
	s_setprio 1
	s_waitcnt lgkmcnt(0)
	v_mfma_f32_16x16x128_f8f6f4 v[154:157], v[26:33], v[174:181], v[154:157]
	v_mfma_f32_16x16x128_f8f6f4 v[158:161], v[18:25], v[174:181], v[158:161]
	v_mfma_f32_16x16x128_f8f6f4 v[138:141], v[26:33], v[182:189], v[138:141]
	v_mfma_f32_16x16x128_f8f6f4 v[130:133], v[18:25], v[182:189], v[130:133]
	v_mfma_f32_16x16x128_f8f6f4 v[126:129], v[26:33], v[194:201], v[126:129]
	v_mfma_f32_16x16x128_f8f6f4 v[122:125], v[18:25], v[194:201], v[122:125]
	v_mfma_f32_16x16x128_f8f6f4 v[110:113], v[26:33], v[214:221], v[110:113]
	v_mfma_f32_16x16x128_f8f6f4 v[106:109], v[18:25], v[214:221], v[106:109]
	s_setprio 0
	s_setprio 1
	v_mfma_f32_16x16x128_f8f6f4 v[146:149], v[10:17], v[174:181], v[146:149]
	v_mfma_f32_16x16x128_f8f6f4 v[150:153], v[2:9], v[174:181], v[150:153]
	v_mfma_f32_16x16x128_f8f6f4 v[142:145], v[10:17], v[182:189], v[142:145]
	v_mfma_f32_16x16x128_f8f6f4 v[134:137], v[2:9], v[182:189], v[134:137]
	v_mfma_f32_16x16x128_f8f6f4 v[118:121], v[10:17], v[194:201], v[118:121]
	v_mfma_f32_16x16x128_f8f6f4 v[114:117], v[2:9], v[194:201], v[114:117]
	v_mfma_f32_16x16x128_f8f6f4 v[94:97], v[10:17], v[214:221], v[94:97]
	v_mfma_f32_16x16x128_f8f6f4 v[90:93], v[2:9], v[214:221], v[90:93]
	s_setprio 0
	s_barrier
	s_add_u32 s8, s40, 0x80
	s_addc_u32 s9, s41, 0
	s_mov_b32 m0, s18
	ds_read_b128 v[174:177], v173 offset:49152
	ds_read_b128 v[178:181], v173 offset:50176
	ds_read_b128 v[182:185], v173 offset:51200
	ds_read_b128 v[186:189], v173 offset:52224
	ds_read_b128 v[194:197], v173 offset:53248
	ds_read_b128 v[198:201], v173 offset:54272
	ds_read_b128 v[214:217], v173 offset:55296
	ds_read_b128 v[218:221], v173 offset:56320
	s_nop 0
	v_lshl_add_u64 v[202:203], s[8:9], 0, v[164:165]
	global_load_lds_dwordx4 v[202:203], off
	v_lshl_add_u64 v[202:203], s[8:9], 0, v[162:163]
	s_add_u32 s8, s40, 0x20080
	s_mov_b32 m0, s19
	s_addc_u32 s9, s41, 0
	global_load_lds_dwordx4 v[202:203], off
	s_mov_b32 m0, s59
	v_lshl_add_u64 v[202:203], s[8:9], 0, v[164:165]
	global_load_lds_dwordx4 v[202:203], off
	v_lshl_add_u64 v[202:203], s[8:9], 0, v[162:163]
	s_mov_b32 m0, s60
	s_nop 0
	global_load_lds_dwordx4 v[202:203], off
	s_mov_b32 m0, s50
	v_lshl_add_u64 v[202:203], s[30:31], 0, v[164:165]
	global_load_lds_dwordx4 v[202:203], off
	v_lshl_add_u64 v[202:203], s[30:31], 0, v[162:163]
	s_mov_b32 m0, s51
	s_nop 0
	global_load_lds_dwordx4 v[202:203], off
	s_waitcnt vmcnt(8)
	s_waitcnt lgkmcnt(0)
	s_barrier
	s_setprio 1
	s_waitcnt lgkmcnt(0)
	v_mfma_f32_16x16x128_f8f6f4 v[102:105], v[26:33], v[174:181], v[102:105]
	v_mfma_f32_16x16x128_f8f6f4 v[98:101], v[18:25], v[174:181], v[98:101]
	v_mfma_f32_16x16x128_f8f6f4 v[78:81], v[26:33], v[182:189], v[78:81]
	v_mfma_f32_16x16x128_f8f6f4 v[74:77], v[18:25], v[182:189], v[74:77]
	v_mfma_f32_16x16x128_f8f6f4 v[62:65], v[26:33], v[194:201], v[62:65]
	v_mfma_f32_16x16x128_f8f6f4 v[58:61], v[18:25], v[194:201], v[58:61]
	v_mfma_f32_16x16x128_f8f6f4 v[46:49], v[26:33], v[214:221], v[46:49]
	v_mfma_f32_16x16x128_f8f6f4 v[42:45], v[18:25], v[214:221], v[42:45]
	s_setprio 0
	s_setprio 1
	v_mfma_f32_16x16x128_f8f6f4 v[86:89], v[10:17], v[174:181], v[86:89]
	v_mfma_f32_16x16x128_f8f6f4 v[82:85], v[2:9], v[174:181], v[82:85]
	v_mfma_f32_16x16x128_f8f6f4 v[70:73], v[10:17], v[182:189], v[70:73]
	v_mfma_f32_16x16x128_f8f6f4 v[66:69], v[2:9], v[182:189], v[66:69]
	v_mfma_f32_16x16x128_f8f6f4 v[54:57], v[10:17], v[194:201], v[54:57]
	v_mfma_f32_16x16x128_f8f6f4 v[50:53], v[2:9], v[194:201], v[50:53]
	v_mfma_f32_16x16x128_f8f6f4 v[38:41], v[10:17], v[214:221], v[38:41]
	v_mfma_f32_16x16x128_f8f6f4 v[34:37], v[2:9], v[214:221], v[34:37]
	s_add_i32 s61, s61, 2
	s_cmp_gt_u32 s61, 5
	s_mov_b64 s[8:9], s[28:29]
	s_setprio 0
	s_barrier
	s_cbranch_scc0 .LBB0_1499
	s_and_b64 vcc, exec, s[4:5]
	s_cbranch_vccz .LBB0_1502
	s_barrier
